# inproj0 and inproj1: XCD-local tile dealing (each XCD owns the M-tiles m = xcd mod 8 and walks their N-tiles)
# baseline (speedup 1.0000x reference)
;     template <int BM> __device__ __forceinline__ void init(const bfr* base, int ld, int row0, int maxrow, const int* ridx) {
; #pragma unroll
;         for (int i = 0; i < (BM * 4 + NTHR - 1) / NTHR; ++i) {
;             const int id = threadIdx.x + i * NTHR, kc = id & 3;
;             int r = id >> 2; if (r > BM - 1) r = BM - 1;
;             int row = ridx ? ridx[r] : row0 + r;
;             if (row > maxrow) row = maxrow;
;             p[i] = base + (size_t)row * ld + kc * 8;
;         }
;     }
;     template <int BN> __device__ __forceinline__ void init(const bfr* base, int ld, int n0) {
; #pragma unroll
;         for (int i = 0; i < BN * 4 / NTHR; ++i) {
;             const int id = threadIdx.x + i * NTHR, r = id >> 2, kc = id & 3;
;             p[i] = base + (size_t)(n0 + r) * ld + kc * 8;
;         }
;     }
; __device__ __forceinline__ void phase_inproj0(const Params& P, bfr* smem, int bid, int nb) {
;     ...
;     constexpr int nu = 65 * 24;
;     GemmPipe<256, 128, 1024, ALoadRows, BLoadT> gp;
;     ALoadRows al; BLoadT bl;
;     int u = bid;
;     if (u < nu) { al.init<256>(A, 1024, (u / 24) * 256, NT - 1, nullptr); bl.init<128>(Bt, 1024, (u % 24) * 128); gp.prefetch(al, bl); }
;     while (u < nu) {
;         EpiInProj0 ep{(bfr*)(P.ws + WS_QKVU), (bfr*)(P.ws + WS_VT0), (bfr*)(P.ws + WS_K0F), (u / 24) * 256, (u % 24) * 128};
;         gp.mainloop(smem, al, bl);
;         const int un = u + nb;
;         if (un < nu) { al.init<256>(A, 1024, (un / 24) * 256, NT - 1, nullptr); bl.init<128>(Bt, 1024, (un % 24) * 128); gp.prefetch(al, bl); }
.LBB0_411:
	s_cmp_lt_i32 s6, 3
	s_cselect_b64 s[0:1], -1, 0
	s_cmp_gt_i32 s7, 2
	s_cselect_b64 s[2:3], -1, 0
	s_and_b64 s[0:1], s[0:1], s[2:3]
	s_andn2_b64 vcc, exec, s[0:1]
	s_cbranch_vccnz .LBB0_481
	v_readlane_b32 s97, v253, 10
	s_cmpk_lg_u32 s97, 0x100
	s_mov_b32 s97, s44
	s_cbranch_scc1 .Lipx_i_2
	s_lshr_b32 s96, s44, 3
	s_mul_i32 s97, s96, 2731
	s_lshr_b32 s97, s97, 16
	s_mul_i32 s97, s97, 168
	s_add_i32 s97, s97, s96
	s_and_b32 s98, s44, 7
	s_mul_i32 s98, s98, 24
	s_add_i32 s97, s97, s98
.Lipx_i_2:
	s_cmpk_gt_i32 s97, 0x617
	s_cbranch_scc1 .LBB0_427
	s_add_u32 s0, s42, 0x28000
	s_mul_hi_i32 s2, s97, 0x2aaaaaab
	v_lshlrev_b32_e32 v1, 3, v0
	s_addc_u32 s1, s43, 0
	s_lshr_b32 s3, s2, 31
	s_ashr_i32 s2, s2, 2
	v_and_b32_e32 v4, 24, v1
	s_add_i32 s4, s2, s3
	v_lshlrev_b32_e32 v110, 1, v4
	v_mov_b32_e32 v111, 0
	s_lshl_b32 s5, s4, 8
	v_lshl_add_u64 v[2:3], s[42:43], 0, v[110:111]
	s_mov_b64 s[2:3], 0x4ff8000
	v_lshrrev_b32_e32 v123, 2, v0
	v_lshl_add_u64 v[112:113], v[2:3], 0, s[2:3]
	v_or_b32_e32 v2, s5, v123
	v_ashrrev_i32_e32 v3, 31, v2
	v_lshlrev_b64 v[2:3], 11, v[2:3]
	v_lshl_add_u64 v[114:115], v[112:113], 0, v[2:3]
	v_or_b32_e32 v2, 0x200, v0
	v_lshrrev_b32_e32 v125, 2, v2
	v_or_b32_e32 v2, s5, v125
	v_ashrrev_i32_e32 v3, 31, v2
	s_mul_i32 s4, s4, 24
	v_lshlrev_b64 v[2:3], 11, v[2:3]
	s_sub_i32 s2, s97, s4
	v_lshl_add_u64 v[116:117], v[112:113], 0, v[2:3]
	v_lshl_or_b32 v2, s2, 7, v123
	v_ashrrev_i32_e32 v3, 31, v2
	v_lshlrev_b64 v[2:3], 11, v[2:3]
	v_lshl_add_u64 v[2:3], s[0:1], 0, v[2:3]
	v_lshl_add_u64 v[118:119], v[2:3], 0, v[110:111]
	global_load_dwordx4 v[78:81], v[116:117], off
	global_load_dwordx4 v[90:93], v[116:117], off offset:64
	global_load_dwordx4 v[82:85], v[118:119], off
	global_load_dwordx4 v[94:97], v[118:119], off offset:64
	global_load_dwordx4 v[98:101], v[114:115], off offset:64
	global_load_dwordx4 v[66:69], v[114:115], off offset:128
	global_load_dwordx4 v[74:77], v[116:117], off offset:128
	global_load_dwordx4 v[86:89], v[114:115], off
	global_load_dwordx4 v[70:73], v[118:119], off offset:128
	v_mad_u32_u24 v3, v125, 40, v4
	v_mul_u32_u24_e32 v2, 40, v123
	v_lshl_add_u32 v129, v3, 1, 0
	v_lshrrev_b32_e32 v3, 1, v0
	v_add_lshl_u32 v2, v2, v4, 1
	v_and_b32_e32 v131, 0xc0, v3
	v_and_b32_e32 v4, 31, v0
	v_or_b32_e32 v5, v131, v4
	v_and_b32_e32 v6, 8, v123
	v_mul_u32_u24_e32 v5, 40, v5
	v_lshl_add_u32 v7, v6, 1, 0
	v_lshl_add_u32 v132, v5, 1, v7
	v_and_b32_e32 v5, 0x5f, v0
	v_mov_b32_e32 v11, 0x500
	v_mul_u32_u24_e32 v8, 0x50, v5
	v_mul_u32_u24_e32 v9, 40, v5
	v_mad_u32_u24 v5, v5, 40, v11
	v_add_lshl_u32 v10, v9, v6, 1
	v_add_lshl_u32 v11, v5, v6, 1
	v_or_b32_e32 v6, 16, v6
	s_add_i32 s2, 0, 0x11810
	v_add_lshl_u32 v12, v6, v9, 1
	v_add_lshl_u32 v5, v5, v6, 1
	v_add_u32_e32 v130, s2, v2
	v_add_u32_e32 v133, s2, v10
	v_add_u32_e32 v134, s2, v11
	v_add_u32_e32 v135, s2, v12
	v_add_u32_e32 v136, s2, v5
	s_add_i32 s2, 0, 0x14010
	v_add_u32_e32 v141, s2, v5
	v_lshrrev_b32_e32 v5, 3, v0
	v_add_u32_e32 v128, 0, v2
	v_add_u32_e32 v137, s2, v2
	v_bfe_u32 v2, v0, 6, 1
	v_and_or_b32 v144, v5, 4, v131
	v_lshl_add_u64 v[120:121], s[0:1], 0, v[110:111]
	v_lshl_add_u32 v6, v2, 8, 0
	v_lshlrev_b32_e32 v4, 2, v4
	v_mul_u32_u24_e32 v5, 0x210, v144
	s_add_u32 s0, s42, 0x7078000
	v_add3_u32 v145, v6, v4, v5
	v_mov_b32_e32 v4, 0xfffffc00
	s_addc_u32 s1, s43, 0
	v_add_u32_e32 v138, s2, v10
	v_add_u32_e32 v139, s2, v11
	v_add_u32_e32 v140, s2, v12
	v_lshl_or_b32 v147, v2, 6, v4
	s_add_u32 s2, s42, 0x3c562400
	v_and_b32_e32 v2, 15, v0
	s_movk_i32 s6, 0x210
	v_lshrrev_b32_e32 v122, 4, v0
	s_addc_u32 s3, s43, 0
	v_lshlrev_b32_e32 v2, 5, v2
	s_add_u32 s4, s42, 0x3f622400
	v_mad_u32_u24 v2, v122, s6, v2
	s_movk_i32 s14, 0xc0
	v_lshl_add_u32 v142, v9, 1, v7
	v_add_u32_e32 v143, 0, v12
	v_or_b32_e32 v146, 16, v131
	v_or_b32_e32 v148, 32, v131
	v_or_b32_e32 v149, 48, v3
	s_addc_u32 s5, s43, 0
	v_or_b32_e32 v124, 64, v202
	v_or_b32_e32 v150, 0xfffffe00, v0
	v_add3_u32 v151, v2, 0, 16
	v_add_u32_e32 v152, v7, v8
	s_movk_i32 s15, 0x1800
	s_movk_i32 s16, 0x208
	s_movk_i32 s17, 0xdff
	s_movk_i32 s18, 0x410
	s_mov_b32 s8, s97
	s_branch .LBB0_415

; #define G_LOAD(SA, SB, KT) do { SA.load(al, (KT) * 32); SB.load(bl, (KT) * 32); } while (0)
; #define G_STORE(SA, SB, BUF) do { SA.store(As + (BUF) * ASZ, tid); SB.store(Bs3 + (BUF) * BSZ, tid); } while (0)
;     __device__ __forceinline__ void mainloop(bfr* smem, const AL& al, const BL& bl) {
;     ...
;         __syncthreads();
;         G_STORE(sa0, sb0, 0);
;         if (1 < nk) G_STORE(sa1, sb1, 1);
;         if (BL::DEPTH < nk) G_LOAD(sa0, sb0, BL::DEPTH);
;         if (BL::DEPTH + 1 < nk) G_LOAD(sa1, sb1, BL::DEPTH + 1);
;         __builtin_amdgcn_sched_barrier(0);
;         __syncthreads();
;         G_RD(fa0, fb0, 0);
;         if constexpr (BL::DEPTH == 3) {
; #pragma unroll
;             for (int kt = 0; kt < nk; kt += 6) {
;                 G_STEP(0, fa0, fb0, fa1, fb1, 1, sa2, sb2, 2, 3);
;                 G_STEP(1, fa1, fb1, fa0, fb0, 2, sa0, sb0, 0, 3);
;                 G_STEP(2, fa0, fb0, fa1, fb1, 0, sa1, sb1, 1, 3);
;                 G_STEP(3, fa1, fb1, fa0, fb0, 1, sa2, sb2, 2, 3);
;                 G_STEP(4, fa0, fb0, fa1, fb1, 2, sa0, sb0, 0, 3);
;                 G_STEP(5, fa1, fb1, fa0, fb0, 0, sa1, sb1, 1, 3);
.LBB0_415:
	s_barrier
	global_load_dwordx4 v[102:105], v[114:115], off offset:192
	global_load_dwordx4 v[106:109], v[114:115], off offset:256
	global_load_dwordx4 v[154:157], v[116:117], off offset:192
	global_load_dwordx4 v[158:161], v[116:117], off offset:256
	global_load_dwordx4 v[162:165], v[118:119], off offset:192
	global_load_dwordx4 v[166:169], v[118:119], off offset:256
	s_waitcnt vmcnt(7)
	ds_write_b128 v128, v[86:89] offset:16
	ds_write_b128 v129, v[78:81] offset:16
	ds_write_b128 v128, v[82:85] offset:61456
	ds_write_b128 v128, v[98:101] offset:20496
	ds_write_b128 v129, v[90:93] offset:20496
	ds_write_b128 v130, v[94:97]
	s_waitcnt lgkmcnt(0)
	s_barrier
	ds_read_b128 v[2:5], v132 offset:16
	ds_read_b128 v[78:81], v132 offset:48
	ds_read_b128 v[6:9], v152 offset:61456
	ds_read_b128 v[10:13], v132 offset:2576
	ds_read_b128 v[82:85], v132 offset:2608
	ds_read_b128 v[86:89], v152 offset:61488
	ds_read_b128 v[14:17], v152 offset:64016
	ds_read_b128 v[90:93], v152 offset:64048
	s_waitcnt lgkmcnt(5)
	v_mfma_f32_32x32x16_bf16 v[50:65], v[2:5], v[6:9], 0
	ds_read_b128 v[94:97], v132 offset:20496
	ds_read_b128 v[98:101], v133
	s_waitcnt lgkmcnt(3)
	v_mfma_f32_32x32x16_bf16 v[34:49], v[2:5], v[14:17], 0
	ds_read_b128 v[170:173], v132 offset:23056
	ds_read_b128 v[174:177], v134
	v_mfma_f32_32x32x16_bf16 v[18:33], v[10:13], v[6:9], 0
	ds_read_b128 v[178:181], v132 offset:20528
	ds_read_b128 v[182:185], v135
	v_mfma_f32_32x32x16_bf16 v[2:17], v[10:13], v[14:17], 0
	ds_read_b128 v[186:189], v132 offset:23088
	ds_read_b128 v[190:193], v136
	v_mfma_f32_32x32x16_bf16 v[50:65], v[78:81], v[86:89], v[50:65]
	ds_write_b128 v128, v[66:69] offset:40976
	ds_write_b128 v129, v[74:77] offset:40976
	s_waitcnt lgkmcnt(10)
	v_mfma_f32_32x32x16_bf16 v[34:49], v[78:81], v[90:93], v[34:49]
	s_waitcnt vmcnt(6)
	ds_write_b128 v137, v[70:73]
	v_mfma_f32_32x32x16_bf16 v[18:33], v[82:85], v[86:89], v[18:33]
	global_load_dwordx4 v[66:69], v[114:115], off offset:320
	global_load_dwordx4 v[70:73], v[116:117], off offset:320
	global_load_dwordx4 v[74:77], v[118:119], off offset:320
	v_mfma_f32_32x32x16_bf16 v[2:17], v[82:85], v[90:93], v[2:17]
	s_waitcnt lgkmcnt(0)
	s_barrier
	v_mfma_f32_32x32x16_bf16 v[50:65], v[94:97], v[98:101], v[50:65]
	ds_read_b128 v[78:81], v132 offset:40976
	ds_read_b128 v[82:85], v138
	v_mfma_f32_32x32x16_bf16 v[34:49], v[94:97], v[174:177], v[34:49]
	ds_read_b128 v[86:89], v132 offset:43536
	ds_read_b128 v[90:93], v139
	v_mfma_f32_32x32x16_bf16 v[18:33], v[170:173], v[98:101], v[18:33]
	ds_read_b128 v[94:97], v132 offset:41008
	ds_read_b128 v[98:101], v140
	v_mfma_f32_32x32x16_bf16 v[2:17], v[170:173], v[174:177], v[2:17]
	ds_read_b128 v[170:173], v132 offset:43568
	ds_read_b128 v[174:177], v141
	v_mfma_f32_32x32x16_bf16 v[50:65], v[178:181], v[182:185], v[50:65]
	s_waitcnt vmcnt(8)
	ds_write_b128 v128, v[102:105] offset:16
	s_waitcnt vmcnt(6)
	ds_write_b128 v129, v[154:157] offset:16
	v_mfma_f32_32x32x16_bf16 v[34:49], v[178:181], v[190:193], v[34:49]
	s_waitcnt vmcnt(4)
	ds_write_b128 v128, v[162:165] offset:61456
	v_mfma_f32_32x32x16_bf16 v[18:33], v[186:189], v[182:185], v[18:33]
	global_load_dwordx4 v[102:105], v[114:115], off offset:384
	global_load_dwordx4 v[154:157], v[116:117], off offset:384
	global_load_dwordx4 v[162:165], v[118:119], off offset:384
	v_mfma_f32_32x32x16_bf16 v[2:17], v[186:189], v[190:193], v[2:17]
	s_waitcnt lgkmcnt(0)
	s_barrier
	v_mfma_f32_32x32x16_bf16 v[50:65], v[78:81], v[82:85], v[50:65]
	ds_read_b128 v[178:181], v132 offset:16
	ds_read_b128 v[182:185], v142 offset:61456
	v_mfma_f32_32x32x16_bf16 v[34:49], v[78:81], v[90:93], v[34:49]
	ds_read_b128 v[78:81], v132 offset:2576
	ds_read_b128 v[186:189], v142 offset:64016
	v_mfma_f32_32x32x16_bf16 v[18:33], v[86:89], v[82:85], v[18:33]
	ds_read_b128 v[82:85], v132 offset:48
	ds_read_b128 v[190:193], v142 offset:61488
	v_mfma_f32_32x32x16_bf16 v[2:17], v[86:89], v[90:93], v[2:17]
	ds_read_b128 v[86:89], v132 offset:2608
	ds_read_b128 v[90:93], v143 offset:64016
	v_mfma_f32_32x32x16_bf16 v[50:65], v[94:97], v[98:101], v[50:65]
	ds_write_b128 v128, v[106:109] offset:20496
	ds_write_b128 v129, v[158:161] offset:20496
	v_mfma_f32_32x32x16_bf16 v[34:49], v[94:97], v[174:177], v[34:49]
	s_waitcnt vmcnt(6)
	ds_write_b128 v130, v[166:169]
	v_mfma_f32_32x32x16_bf16 v[18:33], v[170:173], v[98:101], v[18:33]
	global_load_dwordx4 v[94:97], v[114:115], off offset:448
	global_load_dwordx4 v[98:101], v[116:117], off offset:448
	global_load_dwordx4 v[106:109], v[118:119], off offset:448
	v_mfma_f32_32x32x16_bf16 v[2:17], v[170:173], v[174:177], v[2:17]
	s_waitcnt lgkmcnt(0)
	s_barrier
	v_mfma_f32_32x32x16_bf16 v[50:65], v[178:181], v[182:185], v[50:65]
	ds_read_b128 v[158:161], v132 offset:20496
	ds_read_b128 v[166:169], v133
	v_mfma_f32_32x32x16_bf16 v[34:49], v[178:181], v[186:189], v[34:49]
	ds_read_b128 v[170:173], v132 offset:23056
	ds_read_b128 v[174:177], v134
	v_mfma_f32_32x32x16_bf16 v[18:33], v[78:81], v[182:185], v[18:33]
	ds_read_b128 v[178:181], v132 offset:20528
	ds_read_b128 v[182:185], v135
	v_mfma_f32_32x32x16_bf16 v[2:17], v[78:81], v[186:189], v[2:17]
	ds_read_b128 v[78:81], v132 offset:23088
	ds_read_b128 v[186:189], v136
	v_mfma_f32_32x32x16_bf16 v[50:65], v[82:85], v[190:193], v[50:65]
	s_waitcnt vmcnt(8)
	ds_write_b128 v128, v[66:69] offset:40976
	s_waitcnt vmcnt(7)
	ds_write_b128 v129, v[70:73] offset:40976
	v_mfma_f32_32x32x16_bf16 v[34:49], v[82:85], v[90:93], v[34:49]
	s_waitcnt vmcnt(6)
	ds_write_b128 v137, v[74:77]
	v_mfma_f32_32x32x16_bf16 v[18:33], v[86:89], v[190:193], v[18:33]
	global_load_dwordx4 v[66:69], v[114:115], off offset:512
	global_load_dwordx4 v[70:73], v[116:117], off offset:512
	global_load_dwordx4 v[74:77], v[118:119], off offset:512
	v_mfma_f32_32x32x16_bf16 v[2:17], v[86:89], v[90:93], v[2:17]
	s_waitcnt lgkmcnt(0)
	s_barrier
	v_mfma_f32_32x32x16_bf16 v[50:65], v[158:161], v[166:169], v[50:65]
	ds_read_b128 v[82:85], v132 offset:40976
	ds_read_b128 v[86:89], v138
	v_mfma_f32_32x32x16_bf16 v[34:49], v[158:161], v[174:177], v[34:49]
	ds_read_b128 v[90:93], v132 offset:43536
	ds_read_b128 v[158:161], v139
	v_mfma_f32_32x32x16_bf16 v[18:33], v[170:173], v[166:169], v[18:33]
	ds_read_b128 v[166:169], v132 offset:41008
	ds_read_b128 v[190:193], v140
	v_mfma_f32_32x32x16_bf16 v[2:17], v[170:173], v[174:177], v[2:17]
	ds_read_b128 v[170:173], v132 offset:43568
	ds_read_b128 v[174:177], v141
	v_mfma_f32_32x32x16_bf16 v[50:65], v[178:181], v[182:185], v[50:65]
	s_waitcnt vmcnt(8)
	ds_write_b128 v128, v[102:105] offset:16
	s_waitcnt vmcnt(7)
	ds_write_b128 v129, v[154:157] offset:16
	v_mfma_f32_32x32x16_bf16 v[34:49], v[178:181], v[186:189], v[34:49]
	s_waitcnt vmcnt(6)
	ds_write_b128 v128, v[162:165] offset:61456
	v_mfma_f32_32x32x16_bf16 v[18:33], v[78:81], v[182:185], v[18:33]
	global_load_dwordx4 v[102:105], v[114:115], off offset:576
	global_load_dwordx4 v[154:157], v[116:117], off offset:576
	global_load_dwordx4 v[162:165], v[118:119], off offset:576
	v_mfma_f32_32x32x16_bf16 v[2:17], v[78:81], v[186:189], v[2:17]
	s_waitcnt lgkmcnt(0)
	s_barrier
	v_mfma_f32_32x32x16_bf16 v[50:65], v[82:85], v[86:89], v[50:65]
	ds_read_b128 v[78:81], v132 offset:16
	ds_read_b128 v[178:181], v142 offset:61456
	v_mfma_f32_32x32x16_bf16 v[34:49], v[82:85], v[158:161], v[34:49]
	ds_read_b128 v[82:85], v132 offset:2576
	ds_read_b128 v[182:185], v142 offset:64016
	v_mfma_f32_32x32x16_bf16 v[18:33], v[90:93], v[86:89], v[18:33]
	ds_read_b128 v[86:89], v132 offset:48
	ds_read_b128 v[186:189], v142 offset:61488
	v_mfma_f32_32x32x16_bf16 v[2:17], v[90:93], v[158:161], v[2:17]
	ds_read_b128 v[90:93], v132 offset:2608
	ds_read_b128 v[158:161], v143 offset:64016
	v_mfma_f32_32x32x16_bf16 v[50:65], v[166:169], v[190:193], v[50:65]
	s_waitcnt vmcnt(8)
	ds_write_b128 v128, v[94:97] offset:20496
	s_waitcnt vmcnt(7)
	ds_write_b128 v129, v[98:101] offset:20496
	v_mfma_f32_32x32x16_bf16 v[34:49], v[166:169], v[174:177], v[34:49]
	s_waitcnt vmcnt(6)
	ds_write_b128 v130, v[106:109]
	v_mfma_f32_32x32x16_bf16 v[18:33], v[170:173], v[190:193], v[18:33]
	global_load_dwordx4 v[94:97], v[114:115], off offset:640
	global_load_dwordx4 v[98:101], v[116:117], off offset:640
	global_load_dwordx4 v[106:109], v[118:119], off offset:640
	v_mfma_f32_32x32x16_bf16 v[2:17], v[170:173], v[174:177], v[2:17]
	s_waitcnt lgkmcnt(0)
	s_barrier
	v_mfma_f32_32x32x16_bf16 v[50:65], v[78:81], v[178:181], v[50:65]
	ds_read_b128 v[166:169], v132 offset:20496
	ds_read_b128 v[170:173], v133
	v_mfma_f32_32x32x16_bf16 v[34:49], v[78:81], v[182:185], v[34:49]
	ds_read_b128 v[78:81], v132 offset:23056
	ds_read_b128 v[174:177], v134
	v_mfma_f32_32x32x16_bf16 v[18:33], v[82:85], v[178:181], v[18:33]
	ds_read_b128 v[178:181], v132 offset:20528
	ds_read_b128 v[190:193], v135
	v_mfma_f32_32x32x16_bf16 v[2:17], v[82:85], v[182:185], v[2:17]
	ds_read_b128 v[82:85], v132 offset:23088
	ds_read_b128 v[182:185], v136
	v_mfma_f32_32x32x16_bf16 v[50:65], v[86:89], v[186:189], v[50:65]
	s_waitcnt vmcnt(8)
	ds_write_b128 v128, v[66:69] offset:40976
	s_waitcnt vmcnt(7)
	ds_write_b128 v129, v[70:73] offset:40976
	v_mfma_f32_32x32x16_bf16 v[34:49], v[86:89], v[158:161], v[34:49]
	s_waitcnt vmcnt(6)
	ds_write_b128 v137, v[74:77]
	v_mfma_f32_32x32x16_bf16 v[18:33], v[90:93], v[186:189], v[18:33]
	global_load_dwordx4 v[66:69], v[114:115], off offset:704
	global_load_dwordx4 v[70:73], v[116:117], off offset:704
	global_load_dwordx4 v[74:77], v[118:119], off offset:704
	v_mfma_f32_32x32x16_bf16 v[2:17], v[90:93], v[158:161], v[2:17]
	s_waitcnt lgkmcnt(0)
	s_barrier
	v_mfma_f32_32x32x16_bf16 v[50:65], v[166:169], v[170:173], v[50:65]
	ds_read_b128 v[86:89], v132 offset:40976
	ds_read_b128 v[90:93], v138
	v_mfma_f32_32x32x16_bf16 v[34:49], v[166:169], v[174:177], v[34:49]
	ds_read_b128 v[158:161], v132 offset:43536
	ds_read_b128 v[166:169], v139
	v_mfma_f32_32x32x16_bf16 v[18:33], v[78:81], v[170:173], v[18:33]
	ds_read_b128 v[170:173], v132 offset:41008
	ds_read_b128 v[186:189], v140
	v_mfma_f32_32x32x16_bf16 v[2:17], v[78:81], v[174:177], v[2:17]
	ds_read_b128 v[78:81], v132 offset:43568
	ds_read_b128 v[174:177], v141
	v_mfma_f32_32x32x16_bf16 v[50:65], v[178:181], v[190:193], v[50:65]
	s_waitcnt vmcnt(8)
	ds_write_b128 v128, v[102:105] offset:16
	s_waitcnt vmcnt(7)
	ds_write_b128 v129, v[154:157] offset:16
	v_mfma_f32_32x32x16_bf16 v[34:49], v[178:181], v[182:185], v[34:49]
	s_waitcnt vmcnt(6)
	ds_write_b128 v128, v[162:165] offset:61456
	v_mfma_f32_32x32x16_bf16 v[18:33], v[82:85], v[190:193], v[18:33]
	global_load_dwordx4 v[102:105], v[114:115], off offset:768
	global_load_dwordx4 v[154:157], v[116:117], off offset:768
	global_load_dwordx4 v[162:165], v[118:119], off offset:768
	v_mfma_f32_32x32x16_bf16 v[2:17], v[82:85], v[182:185], v[2:17]
	s_waitcnt lgkmcnt(0)
	s_barrier
	v_mfma_f32_32x32x16_bf16 v[50:65], v[86:89], v[90:93], v[50:65]
	ds_read_b128 v[82:85], v132 offset:16
	ds_read_b128 v[178:181], v142 offset:61456
	v_mfma_f32_32x32x16_bf16 v[34:49], v[86:89], v[166:169], v[34:49]
	ds_read_b128 v[86:89], v132 offset:2576
	ds_read_b128 v[182:185], v142 offset:64016
	v_mfma_f32_32x32x16_bf16 v[18:33], v[158:161], v[90:93], v[18:33]
	ds_read_b128 v[90:93], v132 offset:48
	ds_read_b128 v[190:193], v142 offset:61488
	v_mfma_f32_32x32x16_bf16 v[2:17], v[158:161], v[166:169], v[2:17]
	ds_read_b128 v[158:161], v132 offset:2608
	ds_read_b128 v[166:169], v143 offset:64016
	v_mfma_f32_32x32x16_bf16 v[50:65], v[170:173], v[186:189], v[50:65]
	s_waitcnt vmcnt(8)
	ds_write_b128 v128, v[94:97] offset:20496
	s_waitcnt vmcnt(7)
	ds_write_b128 v129, v[98:101] offset:20496
	v_mfma_f32_32x32x16_bf16 v[34:49], v[170:173], v[174:177], v[34:49]
	s_waitcnt vmcnt(6)
	ds_write_b128 v130, v[106:109]
	v_mfma_f32_32x32x16_bf16 v[18:33], v[78:81], v[186:189], v[18:33]
	global_load_dwordx4 v[94:97], v[114:115], off offset:832
	global_load_dwordx4 v[98:101], v[116:117], off offset:832
	global_load_dwordx4 v[106:109], v[118:119], off offset:832
	v_mfma_f32_32x32x16_bf16 v[2:17], v[78:81], v[174:177], v[2:17]
	s_waitcnt lgkmcnt(0)
	s_barrier
	v_mfma_f32_32x32x16_bf16 v[50:65], v[82:85], v[178:181], v[50:65]
	ds_read_b128 v[78:81], v132 offset:20496
	ds_read_b128 v[170:173], v133
	v_mfma_f32_32x32x16_bf16 v[34:49], v[82:85], v[182:185], v[34:49]
	ds_read_b128 v[82:85], v132 offset:23056
	ds_read_b128 v[174:177], v134
	v_mfma_f32_32x32x16_bf16 v[18:33], v[86:89], v[178:181], v[18:33]
	ds_read_b128 v[178:181], v132 offset:20528
	ds_read_b128 v[186:189], v135
	v_mfma_f32_32x32x16_bf16 v[2:17], v[86:89], v[182:185], v[2:17]
	ds_read_b128 v[86:89], v132 offset:23088
	ds_read_b128 v[182:185], v136
	v_mfma_f32_32x32x16_bf16 v[50:65], v[90:93], v[190:193], v[50:65]
	s_waitcnt vmcnt(8)
	ds_write_b128 v128, v[66:69] offset:40976
	s_waitcnt vmcnt(7)
	ds_write_b128 v129, v[70:73] offset:40976
	v_mfma_f32_32x32x16_bf16 v[34:49], v[90:93], v[166:169], v[34:49]
	s_waitcnt vmcnt(6)
	ds_write_b128 v137, v[74:77]
	v_mfma_f32_32x32x16_bf16 v[18:33], v[158:161], v[190:193], v[18:33]
	global_load_dwordx4 v[66:69], v[114:115], off offset:896
	global_load_dwordx4 v[70:73], v[116:117], off offset:896
	global_load_dwordx4 v[74:77], v[118:119], off offset:896
	v_mfma_f32_32x32x16_bf16 v[2:17], v[158:161], v[166:169], v[2:17]
	s_waitcnt lgkmcnt(0)
	s_barrier
	v_mfma_f32_32x32x16_bf16 v[50:65], v[78:81], v[170:173], v[50:65]
	ds_read_b128 v[90:93], v132 offset:40976
	ds_read_b128 v[158:161], v138
	v_mfma_f32_32x32x16_bf16 v[34:49], v[78:81], v[174:177], v[34:49]
	ds_read_b128 v[78:81], v132 offset:43536
	ds_read_b128 v[166:169], v139
	v_mfma_f32_32x32x16_bf16 v[18:33], v[82:85], v[170:173], v[18:33]
	ds_read_b128 v[170:173], v132 offset:41008
	ds_read_b128 v[190:193], v140
	v_mfma_f32_32x32x16_bf16 v[2:17], v[82:85], v[174:177], v[2:17]
	ds_read_b128 v[82:85], v132 offset:43568
	ds_read_b128 v[174:177], v141
	v_mfma_f32_32x32x16_bf16 v[50:65], v[178:181], v[186:189], v[50:65]
	s_waitcnt vmcnt(8)
	ds_write_b128 v128, v[102:105] offset:16
	s_waitcnt vmcnt(7)
	ds_write_b128 v129, v[154:157] offset:16
	v_mfma_f32_32x32x16_bf16 v[34:49], v[178:181], v[182:185], v[34:49]
	s_waitcnt vmcnt(6)
	ds_write_b128 v128, v[162:165] offset:61456
	v_mfma_f32_32x32x16_bf16 v[18:33], v[86:89], v[186:189], v[18:33]
	global_load_dwordx4 v[102:105], v[114:115], off offset:960
	global_load_dwordx4 v[154:157], v[116:117], off offset:960
	global_load_dwordx4 v[162:165], v[118:119], off offset:960
	v_mfma_f32_32x32x16_bf16 v[2:17], v[86:89], v[182:185], v[2:17]
	s_waitcnt lgkmcnt(0)
	s_barrier
	v_mfma_f32_32x32x16_bf16 v[50:65], v[90:93], v[158:161], v[50:65]
	ds_read_b128 v[86:89], v132 offset:16
	ds_read_b128 v[178:181], v142 offset:61456
	v_mfma_f32_32x32x16_bf16 v[34:49], v[90:93], v[166:169], v[34:49]
	ds_read_b128 v[90:93], v132 offset:2576
	ds_read_b128 v[182:185], v142 offset:64016
	v_mfma_f32_32x32x16_bf16 v[18:33], v[78:81], v[158:161], v[18:33]
	ds_read_b128 v[158:161], v132 offset:48
	ds_read_b128 v[186:189], v142 offset:61488
	v_mfma_f32_32x32x16_bf16 v[2:17], v[78:81], v[166:169], v[2:17]
	ds_read_b128 v[78:81], v132 offset:2608
	ds_read_b128 v[166:169], v143 offset:64016
	v_mfma_f32_32x32x16_bf16 v[50:65], v[170:173], v[190:193], v[50:65]
	s_waitcnt vmcnt(8)
	ds_write_b128 v128, v[94:97] offset:20496
	s_waitcnt vmcnt(7)
	ds_write_b128 v129, v[98:101] offset:20496
	v_mfma_f32_32x32x16_bf16 v[34:49], v[170:173], v[174:177], v[34:49]
	s_waitcnt vmcnt(6)
	ds_write_b128 v130, v[106:109]
	v_mfma_f32_32x32x16_bf16 v[18:33], v[82:85], v[190:193], v[18:33]
	global_load_dwordx4 v[94:97], v[114:115], off offset:1024
	global_load_dwordx4 v[98:101], v[116:117], off offset:1024
	global_load_dwordx4 v[106:109], v[118:119], off offset:1024
	v_mfma_f32_32x32x16_bf16 v[2:17], v[82:85], v[174:177], v[2:17]
	s_waitcnt lgkmcnt(0)
	s_barrier
	v_mfma_f32_32x32x16_bf16 v[50:65], v[86:89], v[178:181], v[50:65]
	ds_read_b128 v[82:85], v132 offset:20496
	ds_read_b128 v[170:173], v133
	v_mfma_f32_32x32x16_bf16 v[34:49], v[86:89], v[182:185], v[34:49]
	ds_read_b128 v[86:89], v132 offset:23056
	ds_read_b128 v[174:177], v134
	v_mfma_f32_32x32x16_bf16 v[18:33], v[90:93], v[178:181], v[18:33]
	ds_read_b128 v[178:181], v132 offset:20528
	ds_read_b128 v[190:193], v135
	v_mfma_f32_32x32x16_bf16 v[2:17], v[90:93], v[182:185], v[2:17]
	ds_read_b128 v[90:93], v132 offset:23088
	ds_read_b128 v[182:185], v136
	v_mfma_f32_32x32x16_bf16 v[50:65], v[158:161], v[186:189], v[50:65]
	s_waitcnt vmcnt(8)
	ds_write_b128 v128, v[66:69] offset:40976
	s_waitcnt vmcnt(7)
	ds_write_b128 v129, v[70:73] offset:40976
	v_mfma_f32_32x32x16_bf16 v[34:49], v[158:161], v[166:169], v[34:49]
	s_waitcnt vmcnt(6)
	ds_write_b128 v137, v[74:77]
	v_mfma_f32_32x32x16_bf16 v[18:33], v[78:81], v[186:189], v[18:33]
	global_load_dwordx4 v[66:69], v[114:115], off offset:1088
	global_load_dwordx4 v[70:73], v[116:117], off offset:1088
	global_load_dwordx4 v[74:77], v[118:119], off offset:1088
	v_mfma_f32_32x32x16_bf16 v[2:17], v[78:81], v[166:169], v[2:17]
	s_waitcnt lgkmcnt(0)
	s_barrier
	v_mfma_f32_32x32x16_bf16 v[50:65], v[82:85], v[170:173], v[50:65]
	ds_read_b128 v[78:81], v132 offset:40976
	ds_read_b128 v[158:161], v138
	v_mfma_f32_32x32x16_bf16 v[34:49], v[82:85], v[174:177], v[34:49]
	ds_read_b128 v[82:85], v132 offset:43536
	ds_read_b128 v[166:169], v139
	v_mfma_f32_32x32x16_bf16 v[18:33], v[86:89], v[170:173], v[18:33]
	ds_read_b128 v[170:173], v132 offset:41008
	ds_read_b128 v[186:189], v140
	v_mfma_f32_32x32x16_bf16 v[2:17], v[86:89], v[174:177], v[2:17]
	ds_read_b128 v[86:89], v132 offset:43568
	ds_read_b128 v[174:177], v141
	v_mfma_f32_32x32x16_bf16 v[50:65], v[178:181], v[190:193], v[50:65]
	s_waitcnt vmcnt(8)
	ds_write_b128 v128, v[102:105] offset:16
	s_waitcnt vmcnt(7)
	ds_write_b128 v129, v[154:157] offset:16
	v_mfma_f32_32x32x16_bf16 v[34:49], v[178:181], v[182:185], v[34:49]
	s_waitcnt vmcnt(6)
	ds_write_b128 v128, v[162:165] offset:61456
	v_mfma_f32_32x32x16_bf16 v[18:33], v[90:93], v[190:193], v[18:33]
	global_load_dwordx4 v[102:105], v[114:115], off offset:1152
	global_load_dwordx4 v[154:157], v[116:117], off offset:1152
	global_load_dwordx4 v[162:165], v[118:119], off offset:1152
	v_mfma_f32_32x32x16_bf16 v[2:17], v[90:93], v[182:185], v[2:17]
	s_waitcnt lgkmcnt(0)
	s_barrier
	v_mfma_f32_32x32x16_bf16 v[50:65], v[78:81], v[158:161], v[50:65]
	ds_read_b128 v[90:93], v132 offset:16
	ds_read_b128 v[178:181], v142 offset:61456
	v_mfma_f32_32x32x16_bf16 v[34:49], v[78:81], v[166:169], v[34:49]
	ds_read_b128 v[78:81], v132 offset:2576
	ds_read_b128 v[182:185], v142 offset:64016
	v_mfma_f32_32x32x16_bf16 v[18:33], v[82:85], v[158:161], v[18:33]
	ds_read_b128 v[158:161], v132 offset:48
	ds_read_b128 v[190:193], v142 offset:61488
	v_mfma_f32_32x32x16_bf16 v[2:17], v[82:85], v[166:169], v[2:17]
	ds_read_b128 v[82:85], v132 offset:2608
	ds_read_b128 v[166:169], v143 offset:64016
	v_mfma_f32_32x32x16_bf16 v[50:65], v[170:173], v[186:189], v[50:65]
	s_waitcnt vmcnt(8)
	ds_write_b128 v128, v[94:97] offset:20496
	s_waitcnt vmcnt(7)
	ds_write_b128 v129, v[98:101] offset:20496
	v_mfma_f32_32x32x16_bf16 v[34:49], v[170:173], v[174:177], v[34:49]
	s_waitcnt vmcnt(6)
	ds_write_b128 v130, v[106:109]
	v_mfma_f32_32x32x16_bf16 v[18:33], v[86:89], v[186:189], v[18:33]
	global_load_dwordx4 v[94:97], v[114:115], off offset:1216
	global_load_dwordx4 v[98:101], v[116:117], off offset:1216
	global_load_dwordx4 v[106:109], v[118:119], off offset:1216
	v_mfma_f32_32x32x16_bf16 v[2:17], v[86:89], v[174:177], v[2:17]
	s_waitcnt lgkmcnt(0)
	s_barrier
	v_mfma_f32_32x32x16_bf16 v[50:65], v[90:93], v[178:181], v[50:65]
	ds_read_b128 v[86:89], v132 offset:20496
	ds_read_b128 v[170:173], v133
	v_mfma_f32_32x32x16_bf16 v[34:49], v[90:93], v[182:185], v[34:49]
	ds_read_b128 v[90:93], v132 offset:23056
	ds_read_b128 v[174:177], v134
	v_mfma_f32_32x32x16_bf16 v[18:33], v[78:81], v[178:181], v[18:33]
	ds_read_b128 v[178:181], v132 offset:20528
	ds_read_b128 v[186:189], v135
	v_mfma_f32_32x32x16_bf16 v[2:17], v[78:81], v[182:185], v[2:17]
	ds_read_b128 v[78:81], v132 offset:23088
	ds_read_b128 v[182:185], v136
	v_mfma_f32_32x32x16_bf16 v[50:65], v[158:161], v[190:193], v[50:65]
	s_waitcnt vmcnt(8)
	ds_write_b128 v128, v[66:69] offset:40976
	s_waitcnt vmcnt(7)
	ds_write_b128 v129, v[70:73] offset:40976
	v_mfma_f32_32x32x16_bf16 v[34:49], v[158:161], v[166:169], v[34:49]
	s_waitcnt vmcnt(6)
	ds_write_b128 v137, v[74:77]
	v_mfma_f32_32x32x16_bf16 v[18:33], v[82:85], v[190:193], v[18:33]
	global_load_dwordx4 v[66:69], v[114:115], off offset:1280
	global_load_dwordx4 v[70:73], v[116:117], off offset:1280
	global_load_dwordx4 v[74:77], v[118:119], off offset:1280
	v_mfma_f32_32x32x16_bf16 v[2:17], v[82:85], v[166:169], v[2:17]
	s_waitcnt lgkmcnt(0)
	s_barrier
	v_mfma_f32_32x32x16_bf16 v[50:65], v[86:89], v[170:173], v[50:65]
	ds_read_b128 v[82:85], v132 offset:40976
	ds_read_b128 v[158:161], v138
	v_mfma_f32_32x32x16_bf16 v[34:49], v[86:89], v[174:177], v[34:49]
	ds_read_b128 v[86:89], v132 offset:43536
	ds_read_b128 v[166:169], v139
	v_mfma_f32_32x32x16_bf16 v[18:33], v[90:93], v[170:173], v[18:33]
	ds_read_b128 v[170:173], v132 offset:41008
	ds_read_b128 v[190:193], v140
	v_mfma_f32_32x32x16_bf16 v[2:17], v[90:93], v[174:177], v[2:17]
	ds_read_b128 v[90:93], v132 offset:43568
	ds_read_b128 v[174:177], v141
	v_mfma_f32_32x32x16_bf16 v[50:65], v[178:181], v[186:189], v[50:65]
	s_waitcnt vmcnt(8)
	ds_write_b128 v128, v[102:105] offset:16
	s_waitcnt vmcnt(7)
	ds_write_b128 v129, v[154:157] offset:16
	v_mfma_f32_32x32x16_bf16 v[34:49], v[178:181], v[182:185], v[34:49]
	s_waitcnt vmcnt(6)
	ds_write_b128 v128, v[162:165] offset:61456
	v_mfma_f32_32x32x16_bf16 v[18:33], v[78:81], v[186:189], v[18:33]
	global_load_dwordx4 v[102:105], v[114:115], off offset:1344
	global_load_dwordx4 v[154:157], v[116:117], off offset:1344
	global_load_dwordx4 v[162:165], v[118:119], off offset:1344
	v_mfma_f32_32x32x16_bf16 v[2:17], v[78:81], v[182:185], v[2:17]
	s_waitcnt lgkmcnt(0)
	s_barrier
	v_mfma_f32_32x32x16_bf16 v[50:65], v[82:85], v[158:161], v[50:65]
	ds_read_b128 v[78:81], v132 offset:16
	ds_read_b128 v[178:181], v142 offset:61456
	v_mfma_f32_32x32x16_bf16 v[34:49], v[82:85], v[166:169], v[34:49]
	ds_read_b128 v[82:85], v132 offset:2576
	ds_read_b128 v[182:185], v142 offset:64016
	v_mfma_f32_32x32x16_bf16 v[18:33], v[86:89], v[158:161], v[18:33]
	ds_read_b128 v[158:161], v132 offset:48
	ds_read_b128 v[186:189], v142 offset:61488
	v_mfma_f32_32x32x16_bf16 v[2:17], v[86:89], v[166:169], v[2:17]
	ds_read_b128 v[86:89], v132 offset:2608
	ds_read_b128 v[166:169], v143 offset:64016
	v_mfma_f32_32x32x16_bf16 v[50:65], v[170:173], v[190:193], v[50:65]
	s_waitcnt vmcnt(8)
	ds_write_b128 v128, v[94:97] offset:20496
	s_waitcnt vmcnt(7)
	ds_write_b128 v129, v[98:101] offset:20496
	v_mfma_f32_32x32x16_bf16 v[34:49], v[170:173], v[174:177], v[34:49]
	s_waitcnt vmcnt(6)
	ds_write_b128 v130, v[106:109]
	v_mfma_f32_32x32x16_bf16 v[18:33], v[90:93], v[190:193], v[18:33]
	global_load_dwordx4 v[94:97], v[114:115], off offset:1408
	global_load_dwordx4 v[98:101], v[116:117], off offset:1408
	global_load_dwordx4 v[106:109], v[118:119], off offset:1408
	v_mfma_f32_32x32x16_bf16 v[2:17], v[90:93], v[174:177], v[2:17]
	s_waitcnt lgkmcnt(0)
	s_barrier
	v_mfma_f32_32x32x16_bf16 v[50:65], v[78:81], v[178:181], v[50:65]
	ds_read_b128 v[90:93], v132 offset:20496
	ds_read_b128 v[170:173], v133
	v_mfma_f32_32x32x16_bf16 v[34:49], v[78:81], v[182:185], v[34:49]
	ds_read_b128 v[78:81], v132 offset:23056
	ds_read_b128 v[174:177], v134
	v_mfma_f32_32x32x16_bf16 v[18:33], v[82:85], v[178:181], v[18:33]
	ds_read_b128 v[178:181], v132 offset:20528
	ds_read_b128 v[190:193], v135
	v_mfma_f32_32x32x16_bf16 v[2:17], v[82:85], v[182:185], v[2:17]
	ds_read_b128 v[82:85], v132 offset:23088
	ds_read_b128 v[182:185], v136
	v_mfma_f32_32x32x16_bf16 v[50:65], v[158:161], v[186:189], v[50:65]
	s_waitcnt vmcnt(8)
	ds_write_b128 v128, v[66:69] offset:40976
	s_waitcnt vmcnt(7)
	ds_write_b128 v129, v[70:73] offset:40976
	v_mfma_f32_32x32x16_bf16 v[34:49], v[158:161], v[166:169], v[34:49]
	s_waitcnt vmcnt(6)
	ds_write_b128 v137, v[74:77]
	v_mfma_f32_32x32x16_bf16 v[18:33], v[86:89], v[186:189], v[18:33]
	global_load_dwordx4 v[66:69], v[114:115], off offset:1472
	global_load_dwordx4 v[70:73], v[116:117], off offset:1472
	global_load_dwordx4 v[74:77], v[118:119], off offset:1472
	v_mfma_f32_32x32x16_bf16 v[2:17], v[86:89], v[166:169], v[2:17]
	s_waitcnt lgkmcnt(0)
	s_barrier
	v_mfma_f32_32x32x16_bf16 v[50:65], v[90:93], v[170:173], v[50:65]
	ds_read_b128 v[86:89], v132 offset:40976
	ds_read_b128 v[158:161], v138
	v_mfma_f32_32x32x16_bf16 v[34:49], v[90:93], v[174:177], v[34:49]
	ds_read_b128 v[90:93], v132 offset:43536
	ds_read_b128 v[166:169], v139
	v_mfma_f32_32x32x16_bf16 v[18:33], v[78:81], v[170:173], v[18:33]
	ds_read_b128 v[170:173], v132 offset:41008
	ds_read_b128 v[186:189], v140
	v_mfma_f32_32x32x16_bf16 v[2:17], v[78:81], v[174:177], v[2:17]
	ds_read_b128 v[78:81], v132 offset:43568
	ds_read_b128 v[174:177], v141
	v_mfma_f32_32x32x16_bf16 v[50:65], v[178:181], v[190:193], v[50:65]
	s_waitcnt vmcnt(8)
	ds_write_b128 v128, v[102:105] offset:16
	s_waitcnt vmcnt(7)
	ds_write_b128 v129, v[154:157] offset:16
	v_mfma_f32_32x32x16_bf16 v[34:49], v[178:181], v[182:185], v[34:49]
	s_waitcnt vmcnt(6)
	ds_write_b128 v128, v[162:165] offset:61456
	v_mfma_f32_32x32x16_bf16 v[18:33], v[82:85], v[190:193], v[18:33]
	global_load_dwordx4 v[102:105], v[114:115], off offset:1536
	global_load_dwordx4 v[154:157], v[116:117], off offset:1536
	global_load_dwordx4 v[162:165], v[118:119], off offset:1536
	v_mfma_f32_32x32x16_bf16 v[2:17], v[82:85], v[182:185], v[2:17]
	s_waitcnt lgkmcnt(0)
	s_barrier
	v_mfma_f32_32x32x16_bf16 v[50:65], v[86:89], v[158:161], v[50:65]
	ds_read_b128 v[82:85], v132 offset:16
	ds_read_b128 v[178:181], v142 offset:61456
	v_mfma_f32_32x32x16_bf16 v[34:49], v[86:89], v[166:169], v[34:49]
	ds_read_b128 v[86:89], v132 offset:2576
	ds_read_b128 v[182:185], v142 offset:64016
	v_mfma_f32_32x32x16_bf16 v[18:33], v[90:93], v[158:161], v[18:33]
	ds_read_b128 v[158:161], v132 offset:48
	ds_read_b128 v[190:193], v142 offset:61488
	v_mfma_f32_32x32x16_bf16 v[2:17], v[90:93], v[166:169], v[2:17]
	ds_read_b128 v[90:93], v132 offset:2608
	ds_read_b128 v[166:169], v143 offset:64016
	v_mfma_f32_32x32x16_bf16 v[50:65], v[170:173], v[186:189], v[50:65]
	s_waitcnt vmcnt(8)
	ds_write_b128 v128, v[94:97] offset:20496
	s_waitcnt vmcnt(7)
	ds_write_b128 v129, v[98:101] offset:20496
	v_mfma_f32_32x32x16_bf16 v[34:49], v[170:173], v[174:177], v[34:49]
	s_waitcnt vmcnt(6)
	ds_write_b128 v130, v[106:109]
	v_mfma_f32_32x32x16_bf16 v[18:33], v[78:81], v[186:189], v[18:33]
	global_load_dwordx4 v[94:97], v[114:115], off offset:1600
	global_load_dwordx4 v[98:101], v[116:117], off offset:1600
	global_load_dwordx4 v[106:109], v[118:119], off offset:1600
	v_mfma_f32_32x32x16_bf16 v[2:17], v[78:81], v[174:177], v[2:17]
	s_waitcnt lgkmcnt(0)
	s_barrier
	v_mfma_f32_32x32x16_bf16 v[50:65], v[82:85], v[178:181], v[50:65]
	ds_read_b128 v[78:81], v132 offset:20496
	ds_read_b128 v[170:173], v133
	v_mfma_f32_32x32x16_bf16 v[34:49], v[82:85], v[182:185], v[34:49]
	ds_read_b128 v[82:85], v132 offset:23056
	ds_read_b128 v[174:177], v134
	v_mfma_f32_32x32x16_bf16 v[18:33], v[86:89], v[178:181], v[18:33]
	ds_read_b128 v[178:181], v132 offset:20528
	ds_read_b128 v[186:189], v135
	v_mfma_f32_32x32x16_bf16 v[2:17], v[86:89], v[182:185], v[2:17]
	ds_read_b128 v[86:89], v132 offset:23088
	ds_read_b128 v[182:185], v136
	v_mfma_f32_32x32x16_bf16 v[50:65], v[158:161], v[190:193], v[50:65]
	s_waitcnt vmcnt(8)
	ds_write_b128 v128, v[66:69] offset:40976
	s_waitcnt vmcnt(7)
	ds_write_b128 v129, v[70:73] offset:40976
	v_mfma_f32_32x32x16_bf16 v[34:49], v[158:161], v[166:169], v[34:49]
	s_waitcnt vmcnt(6)
	ds_write_b128 v137, v[74:77]
	v_mfma_f32_32x32x16_bf16 v[18:33], v[90:93], v[190:193], v[18:33]
	global_load_dwordx4 v[66:69], v[114:115], off offset:1664
	global_load_dwordx4 v[70:73], v[116:117], off offset:1664
	global_load_dwordx4 v[74:77], v[118:119], off offset:1664
	v_mfma_f32_32x32x16_bf16 v[2:17], v[90:93], v[166:169], v[2:17]
	s_waitcnt lgkmcnt(0)
	s_barrier
	v_mfma_f32_32x32x16_bf16 v[50:65], v[78:81], v[170:173], v[50:65]
	ds_read_b128 v[90:93], v132 offset:40976
	ds_read_b128 v[158:161], v138
	v_mfma_f32_32x32x16_bf16 v[34:49], v[78:81], v[174:177], v[34:49]
	ds_read_b128 v[78:81], v132 offset:43536
	ds_read_b128 v[166:169], v139
	v_mfma_f32_32x32x16_bf16 v[18:33], v[82:85], v[170:173], v[18:33]
	ds_read_b128 v[170:173], v132 offset:41008
	ds_read_b128 v[190:193], v140
	v_mfma_f32_32x32x16_bf16 v[2:17], v[82:85], v[174:177], v[2:17]
	ds_read_b128 v[82:85], v132 offset:43568
	ds_read_b128 v[174:177], v141
	v_mfma_f32_32x32x16_bf16 v[50:65], v[178:181], v[186:189], v[50:65]
	s_waitcnt vmcnt(8)
	ds_write_b128 v128, v[102:105] offset:16
	s_waitcnt vmcnt(7)
	ds_write_b128 v129, v[154:157] offset:16
	v_mfma_f32_32x32x16_bf16 v[34:49], v[178:181], v[182:185], v[34:49]
	s_waitcnt vmcnt(6)
	ds_write_b128 v128, v[162:165] offset:61456
	v_mfma_f32_32x32x16_bf16 v[18:33], v[86:89], v[186:189], v[18:33]
	global_load_dwordx4 v[102:105], v[114:115], off offset:1728
	global_load_dwordx4 v[154:157], v[116:117], off offset:1728
	global_load_dwordx4 v[162:165], v[118:119], off offset:1728
	v_mfma_f32_32x32x16_bf16 v[2:17], v[86:89], v[182:185], v[2:17]
	s_waitcnt lgkmcnt(0)
	s_barrier
	v_mfma_f32_32x32x16_bf16 v[50:65], v[90:93], v[158:161], v[50:65]
	ds_read_b128 v[86:89], v132 offset:16
	ds_read_b128 v[178:181], v142 offset:61456
	v_mfma_f32_32x32x16_bf16 v[34:49], v[90:93], v[166:169], v[34:49]
	ds_read_b128 v[90:93], v132 offset:2576
	ds_read_b128 v[182:185], v142 offset:64016
	v_mfma_f32_32x32x16_bf16 v[18:33], v[78:81], v[158:161], v[18:33]
	ds_read_b128 v[158:161], v132 offset:48
	ds_read_b128 v[186:189], v142 offset:61488
	v_mfma_f32_32x32x16_bf16 v[2:17], v[78:81], v[166:169], v[2:17]
	ds_read_b128 v[78:81], v132 offset:2608
	ds_read_b128 v[166:169], v143 offset:64016
	v_mfma_f32_32x32x16_bf16 v[50:65], v[170:173], v[190:193], v[50:65]
	s_waitcnt vmcnt(8)
	ds_write_b128 v128, v[94:97] offset:20496
	s_waitcnt vmcnt(7)
	ds_write_b128 v129, v[98:101] offset:20496
	v_mfma_f32_32x32x16_bf16 v[34:49], v[170:173], v[174:177], v[34:49]
	s_waitcnt vmcnt(6)
	ds_write_b128 v130, v[106:109]
	v_mfma_f32_32x32x16_bf16 v[18:33], v[82:85], v[190:193], v[18:33]
	global_load_dwordx4 v[94:97], v[114:115], off offset:1792
	global_load_dwordx4 v[98:101], v[116:117], off offset:1792
	global_load_dwordx4 v[106:109], v[118:119], off offset:1792
	v_mfma_f32_32x32x16_bf16 v[2:17], v[82:85], v[174:177], v[2:17]
	s_waitcnt lgkmcnt(0)
	s_barrier
	v_mfma_f32_32x32x16_bf16 v[50:65], v[86:89], v[178:181], v[50:65]
	ds_read_b128 v[82:85], v132 offset:20496
	ds_read_b128 v[170:173], v133
	v_mfma_f32_32x32x16_bf16 v[34:49], v[86:89], v[182:185], v[34:49]
	ds_read_b128 v[86:89], v132 offset:23056
	ds_read_b128 v[174:177], v134
	v_mfma_f32_32x32x16_bf16 v[18:33], v[90:93], v[178:181], v[18:33]
	ds_read_b128 v[178:181], v132 offset:20528
	ds_read_b128 v[190:193], v135
	v_mfma_f32_32x32x16_bf16 v[2:17], v[90:93], v[182:185], v[2:17]
	ds_read_b128 v[90:93], v132 offset:23088
	ds_read_b128 v[182:185], v136
	v_mfma_f32_32x32x16_bf16 v[50:65], v[158:161], v[186:189], v[50:65]
	s_waitcnt vmcnt(8)
	ds_write_b128 v128, v[66:69] offset:40976
	s_waitcnt vmcnt(7)
	ds_write_b128 v129, v[70:73] offset:40976
	v_mfma_f32_32x32x16_bf16 v[34:49], v[158:161], v[166:169], v[34:49]
	s_waitcnt vmcnt(6)
	ds_write_b128 v137, v[74:77]
	v_mfma_f32_32x32x16_bf16 v[18:33], v[78:81], v[186:189], v[18:33]
	global_load_dwordx4 v[66:69], v[114:115], off offset:1856
	global_load_dwordx4 v[74:77], v[116:117], off offset:1856
	global_load_dwordx4 v[70:73], v[118:119], off offset:1856
	v_mfma_f32_32x32x16_bf16 v[2:17], v[78:81], v[166:169], v[2:17]
	s_waitcnt lgkmcnt(0)
	s_barrier
	v_mfma_f32_32x32x16_bf16 v[50:65], v[82:85], v[170:173], v[50:65]
	ds_read_b128 v[158:161], v132 offset:40976
	ds_read_b128 v[166:169], v138
	v_mfma_f32_32x32x16_bf16 v[34:49], v[82:85], v[174:177], v[34:49]
	ds_read_b128 v[186:189], v132 offset:43536
	ds_read_b128 v[194:197], v139
	v_mfma_f32_32x32x16_bf16 v[18:33], v[86:89], v[170:173], v[18:33]
	ds_read_b128 v[170:173], v132 offset:41008
	ds_read_b128 v[198:201], v140
	v_mfma_f32_32x32x16_bf16 v[2:17], v[86:89], v[174:177], v[2:17]
	ds_read_b128 v[174:177], v132 offset:43568
	ds_read_b128 v[204:207], v141
	v_mfma_f32_32x32x16_bf16 v[50:65], v[178:181], v[190:193], v[50:65]
	s_waitcnt vmcnt(8)
	ds_write_b128 v128, v[102:105] offset:16
	s_waitcnt vmcnt(7)
	ds_write_b128 v129, v[154:157] offset:16
	v_mfma_f32_32x32x16_bf16 v[34:49], v[178:181], v[182:185], v[34:49]
	s_waitcnt vmcnt(6)
	ds_write_b128 v128, v[162:165] offset:61456
	v_mfma_f32_32x32x16_bf16 v[18:33], v[90:93], v[190:193], v[18:33]
	global_load_dwordx4 v[86:89], v[114:115], off offset:1920
	global_load_dwordx4 v[78:81], v[116:117], off offset:1920
	global_load_dwordx4 v[82:85], v[118:119], off offset:1920
	v_mfma_f32_32x32x16_bf16 v[2:17], v[90:93], v[182:185], v[2:17]
	s_waitcnt lgkmcnt(0)
	s_barrier
	v_mfma_f32_32x32x16_bf16 v[50:65], v[158:161], v[166:169], v[50:65]
	ds_read_b128 v[102:105], v132 offset:16
	ds_read_b128 v[154:157], v142 offset:61456
	v_mfma_f32_32x32x16_bf16 v[34:49], v[158:161], v[194:197], v[34:49]
	ds_read_b128 v[158:161], v132 offset:2576
	ds_read_b128 v[162:165], v142 offset:64016
	v_mfma_f32_32x32x16_bf16 v[18:33], v[186:189], v[166:169], v[18:33]
	ds_read_b128 v[166:169], v132 offset:48
	ds_read_b128 v[178:181], v142 offset:61488
	v_mfma_f32_32x32x16_bf16 v[2:17], v[186:189], v[194:197], v[2:17]
	ds_read_b128 v[182:185], v132 offset:2608
	ds_read_b128 v[186:189], v143 offset:64016
	v_mfma_f32_32x32x16_bf16 v[50:65], v[170:173], v[198:201], v[50:65]
	s_waitcnt vmcnt(8)
	ds_write_b128 v128, v[94:97] offset:20496
	s_waitcnt vmcnt(7)
	ds_write_b128 v129, v[98:101] offset:20496
	v_mfma_f32_32x32x16_bf16 v[34:49], v[170:173], v[204:207], v[34:49]
	s_waitcnt vmcnt(6)
	ds_write_b128 v130, v[106:109]
	v_mfma_f32_32x32x16_bf16 v[18:33], v[174:177], v[198:201], v[18:33]
	global_load_dwordx4 v[98:101], v[114:115], off offset:1984
	global_load_dwordx4 v[90:93], v[116:117], off offset:1984
	global_load_dwordx4 v[94:97], v[118:119], off offset:1984
	v_mfma_f32_32x32x16_bf16 v[2:17], v[174:177], v[204:207], v[2:17]
	s_waitcnt lgkmcnt(0)
	s_barrier
	v_mfma_f32_32x32x16_bf16 v[50:65], v[102:105], v[154:157], v[50:65]
	ds_read_b128 v[106:109], v132 offset:20496
	ds_read_b128 v[170:173], v133
	v_mfma_f32_32x32x16_bf16 v[34:49], v[102:105], v[162:165], v[34:49]
	ds_read_b128 v[102:105], v132 offset:23056
	ds_read_b128 v[174:177], v134
	v_mfma_f32_32x32x16_bf16 v[18:33], v[158:161], v[154:157], v[18:33]
	ds_read_b128 v[154:157], v132 offset:20528
	ds_read_b128 v[190:193], v135
	v_mfma_f32_32x32x16_bf16 v[2:17], v[158:161], v[162:165], v[2:17]
	ds_read_b128 v[158:161], v132 offset:23088
	ds_read_b128 v[162:165], v136
	v_mfma_f32_32x32x16_bf16 v[50:65], v[166:169], v[178:181], v[50:65]
	s_waitcnt vmcnt(8)
	ds_write_b128 v128, v[66:69] offset:40976
	s_waitcnt vmcnt(7)
	ds_write_b128 v129, v[74:77] offset:40976
	v_mfma_f32_32x32x16_bf16 v[34:49], v[166:169], v[186:189], v[34:49]
	s_waitcnt vmcnt(6)
	ds_write_b128 v137, v[70:73]
	v_mfma_f32_32x32x16_bf16 v[18:33], v[182:185], v[178:181], v[18:33]
	v_mfma_f32_32x32x16_bf16 v[2:17], v[182:185], v[186:189], v[2:17]
	s_waitcnt lgkmcnt(0)
	s_barrier
; __device__ __forceinline__ void phase_inproj0(const Params& P, bfr* smem, int bid, int nb) {
;     ...
;         gp.mainloop(smem, al, bl);
;         const int un = u + nb;
;         if (un < nu) { al.init<256>(A, 1024, (un / 24) * 256, NT - 1, nullptr); bl.init<128>(Bt, 1024, (un % 24) * 128); gp.prefetch(al, bl); }
	v_mfma_f32_32x32x16_bf16 v[50:65], v[106:109], v[170:173], v[50:65]
	ds_read_b128 v[166:169], v132 offset:40976
	ds_read_b128 v[178:181], v138
	v_mfma_f32_32x32x16_bf16 v[34:49], v[106:109], v[174:177], v[34:49]
	ds_read_b128 v[106:109], v132 offset:43536
	ds_read_b128 v[182:185], v139
	v_mfma_f32_32x32x16_bf16 v[18:33], v[102:105], v[170:173], v[18:33]
	ds_read_b128 v[170:173], v132 offset:41008
	ds_read_b128 v[186:189], v140
	v_mfma_f32_32x32x16_bf16 v[2:17], v[102:105], v[174:177], v[2:17]
	ds_read_b128 v[102:105], v132 offset:43568
	ds_read_b128 v[174:177], v141
	v_mfma_f32_32x32x16_bf16 v[50:65], v[154:157], v[190:193], v[50:65]
	s_waitcnt vmcnt(5)
	ds_write_b128 v128, v[86:89] offset:16
	s_waitcnt vmcnt(4)
	ds_write_b128 v129, v[78:81] offset:16
	v_mfma_f32_32x32x16_bf16 v[34:49], v[154:157], v[162:165], v[34:49]
	s_waitcnt vmcnt(3)
	ds_write_b128 v128, v[82:85] offset:61456
	v_mfma_f32_32x32x16_bf16 v[18:33], v[158:161], v[190:193], v[18:33]
	v_mfma_f32_32x32x16_bf16 v[2:17], v[158:161], v[162:165], v[2:17]
	s_waitcnt lgkmcnt(0)
	s_barrier
	v_mfma_f32_32x32x16_bf16 v[50:65], v[166:169], v[178:181], v[50:65]
	ds_read_b128 v[154:157], v132 offset:16
	ds_read_b128 v[158:161], v142 offset:61456
	v_mfma_f32_32x32x16_bf16 v[34:49], v[166:169], v[182:185], v[34:49]
	ds_read_b128 v[162:165], v132 offset:2576
	ds_read_b128 v[166:169], v142 offset:64016
	v_mfma_f32_32x32x16_bf16 v[18:33], v[106:109], v[178:181], v[18:33]
	ds_read_b128 v[178:181], v132 offset:48
	ds_read_b128 v[190:193], v142 offset:61488
	v_mfma_f32_32x32x16_bf16 v[2:17], v[106:109], v[182:185], v[2:17]
	ds_read_b128 v[106:109], v132 offset:2608
	ds_read_b128 v[182:185], v143 offset:64016
	v_mfma_f32_32x32x16_bf16 v[50:65], v[170:173], v[186:189], v[50:65]
	s_waitcnt vmcnt(2)
	ds_write_b128 v128, v[98:101] offset:20496
	s_waitcnt vmcnt(1)
	ds_write_b128 v129, v[90:93] offset:20496
	v_mfma_f32_32x32x16_bf16 v[34:49], v[170:173], v[174:177], v[34:49]
	s_waitcnt vmcnt(0)
	ds_write_b128 v130, v[94:97]
	v_mfma_f32_32x32x16_bf16 v[18:33], v[102:105], v[186:189], v[18:33]
	v_mfma_f32_32x32x16_bf16 v[2:17], v[102:105], v[174:177], v[2:17]
	s_waitcnt lgkmcnt(0)
	s_barrier
	v_mfma_f32_32x32x16_bf16 v[50:65], v[154:157], v[158:161], v[50:65]
	ds_read_b128 v[102:105], v132 offset:20496
	ds_read_b128 v[170:173], v133
	v_mfma_f32_32x32x16_bf16 v[34:49], v[154:157], v[166:169], v[34:49]
	ds_read_b128 v[154:157], v132 offset:23056
	ds_read_b128 v[174:177], v134
	v_mfma_f32_32x32x16_bf16 v[18:33], v[162:165], v[158:161], v[18:33]
	ds_read_b128 v[158:161], v132 offset:20528
	ds_read_b128 v[186:189], v135
	v_mfma_f32_32x32x16_bf16 v[2:17], v[162:165], v[166:169], v[2:17]
	ds_read_b128 v[162:165], v132 offset:23088
	ds_read_b128 v[166:169], v136
	v_mfma_f32_32x32x16_bf16 v[50:65], v[178:181], v[190:193], v[50:65]
	v_mfma_f32_32x32x16_bf16 v[34:49], v[178:181], v[182:185], v[34:49]
	v_mfma_f32_32x32x16_bf16 v[18:33], v[106:109], v[190:193], v[18:33]
	v_mfma_f32_32x32x16_bf16 v[2:17], v[106:109], v[182:185], v[2:17]
	s_waitcnt lgkmcnt(0)
	s_barrier
	v_mfma_f32_32x32x16_bf16 v[50:65], v[102:105], v[170:173], v[50:65]
	v_mfma_f32_32x32x16_bf16 v[34:49], v[102:105], v[174:177], v[34:49]
	v_mfma_f32_32x32x16_bf16 v[18:33], v[154:157], v[170:173], v[18:33]
	v_mfma_f32_32x32x16_bf16 v[2:17], v[154:157], v[174:177], v[2:17]
	v_mfma_f32_32x32x16_bf16 v[50:65], v[158:161], v[186:189], v[50:65]
	v_mfma_f32_32x32x16_bf16 v[34:49], v[158:161], v[166:169], v[34:49]
	v_mfma_f32_32x32x16_bf16 v[18:33], v[162:165], v[186:189], v[18:33]
	v_mfma_f32_32x32x16_bf16 v[2:17], v[162:165], v[166:169], v[2:17]
	v_readlane_b32 s6, v253, 10
	s_add_i32 s19, s8, s6
	s_cmpk_lg_u32 s6, 0x100
	s_cbranch_scc1 .Lipx_u_2
	s_add_i32 s96, s96, 32
	s_mul_i32 s19, s96, 2731
	s_lshr_b32 s19, s19, 16
	s_mul_i32 s19, s19, 168
	s_add_i32 s19, s19, s96
	s_and_b32 s98, s44, 7
	s_mul_i32 s98, s98, 24
	s_add_i32 s19, s19, s98
.Lipx_u_2:
	v_readlane_b32 s7, v253, 11
	s_cmpk_gt_i32 s19, 0x617
	s_cselect_b64 s[6:7], -1, 0
	s_and_b64 vcc, exec, s[6:7]
	s_barrier
	s_cbranch_vccnz .LBB0_417
	s_mul_hi_i32 s9, s19, 0x2aaaaaab
	s_lshr_b32 s10, s9, 31
	s_ashr_i32 s9, s9, 2
	s_add_i32 s9, s9, s10
	s_lshl_b32 s10, s9, 8
	v_or_b32_e32 v66, s10, v123
	v_ashrrev_i32_e32 v67, 31, v66
	v_lshlrev_b64 v[66:67], 11, v[66:67]
	v_lshl_add_u64 v[114:115], v[112:113], 0, v[66:67]
	v_or_b32_e32 v66, s10, v125
	v_ashrrev_i32_e32 v67, 31, v66
	s_mul_i32 s9, s9, 24
	v_lshlrev_b64 v[66:67], 11, v[66:67]
	s_sub_i32 s9, s19, s9
	v_lshl_add_u64 v[116:117], v[112:113], 0, v[66:67]
	v_lshl_or_b32 v66, s9, 7, v123
	v_ashrrev_i32_e32 v67, 31, v66
	v_lshlrev_b64 v[66:67], 11, v[66:67]
	v_lshl_add_u64 v[118:119], v[120:121], 0, v[66:67]
	global_load_dwordx4 v[78:81], v[116:117], off
	global_load_dwordx4 v[90:93], v[116:117], off offset:64
	global_load_dwordx4 v[82:85], v[118:119], off
	global_load_dwordx4 v[94:97], v[118:119], off offset:64
	global_load_dwordx4 v[98:101], v[114:115], off offset:64
	global_load_dwordx4 v[66:69], v[114:115], off offset:128
	global_load_dwordx4 v[74:77], v[116:117], off offset:128
	global_load_dwordx4 v[86:89], v[114:115], off
	global_load_dwordx4 v[70:73], v[118:119], off offset:128

; #define SEAM(k) do { if (P.lo <= (k) && (k) + 1 < P.hi) xcd_barrier(bar); } while (0)
; #define SEAM(k) do { } while (0)
; __device__ __forceinline__ void phase_gemm_bf16out(const bfr* A, int lda, int m0, int M, const bfr* Bt, int N, int K, bfr* C, int ldc, bfr* smem, int bid, int nb) {
;     const int mt = (M + 255) / 256, nt = N / 128, nu = mt * nt;
;     GemmPipe<256, 128, 1024, ALoadRows, BLoadT> gp;
;     ALoadRows al; BLoadT bl;
;     int u = bid;
;     if (u < nu) { al.init<256>(A, lda, m0 + (u / nt) * 256, m0 + M - 1, nullptr); bl.init<128>(Bt, K, (u % nt) * 128); gp.prefetch(al, bl); }
;     while (u < nu) {
;         EpiBf16 ep{C, ldc, m0 + (u / nt) * 256, (u % nt) * 128, m0 + M - 1};
;         gp.mainloop(smem, al, bl);
;         const int un = u + nb;
;         if (un < nu) { al.init<256>(A, lda, m0 + (un / nt) * 256, m0 + M - 1, nullptr); bl.init<128>(Bt, K, (un % nt) * 128); gp.prefetch(al, bl); }
; __global__ void __launch_bounds__(NTHR, 2) fwd_kernel(Params P) {
;     ...
;     if (IN(10)) { phase_gemm_bf16out((const bfr*)(P.ws + WS_H), 1024, 0, NT, (const bfr*)(P.ws + WS_WINT1), 1280, 1024, (bfr*)(P.ws + WS_QKVU), 1280, gsm, bid, nb); if (PROBE_DUP == 10) { phase_gemm_bf16out((const bfr*)(P.ws + WS_H), 1024, 0, NT, (const bfr*)(P.ws + WS_WINT1), 1280, 1024, (bfr*)(P.ws + WS_QKVU), 1280, gsm, bid, nb); } SEAM(10); }
.LBB0_1738:
	s_cmp_lt_i32 s6, 11
	s_cselect_b64 s[0:1], -1, 0
	s_cmp_gt_i32 s7, 10
	s_cselect_b64 s[2:3], -1, 0
	s_and_b64 s[0:1], s[0:1], s[2:3]
	s_andn2_b64 vcc, exec, s[0:1]
	s_cbranch_vccnz .LBB0_1802
	v_readlane_b32 s97, v253, 10
	s_cmpk_lg_u32 s97, 0x100
	s_mov_b32 s97, s44
	s_cbranch_scc1 .Lipx_i_10
	s_lshr_b32 s96, s44, 3
	s_mul_i32 s97, s96, 6554
	s_lshr_b32 s97, s97, 16
	s_mul_i32 s97, s97, 70
	s_add_i32 s97, s97, s96
	s_and_b32 s98, s44, 7
	s_mul_i32 s98, s98, 10
	s_add_i32 s97, s97, s98
.Lipx_i_10:
	s_cmpk_gt_i32 s97, 0x289
	s_cbranch_scc1 .LBB0_1748
	s_add_u32 s8, s42, 0x7078000
	s_addc_u32 s9, s43, 0
	s_add_u32 s0, s42, 0x828000
	s_mul_hi_i32 s2, s97, 0x66666667
	v_lshlrev_b32_e32 v1, 3, v0
	s_addc_u32 s1, s43, 0
	s_lshr_b32 s3, s2, 31
	s_ashr_i32 s2, s2, 2
	v_and_b32_e32 v4, 24, v1
	s_add_i32 s4, s2, s3
	s_waitcnt vmcnt(4)
	v_lshlrev_b32_e32 v102, 1, v4
	v_mov_b32_e32 v103, 0
	s_lshl_b32 s5, s4, 8
	v_lshl_add_u64 v[2:3], s[42:43], 0, v[102:103]
	s_mov_b64 s[2:3], 0x4ff8000
	v_lshrrev_b32_e32 v114, 2, v0
	v_lshl_add_u64 v[104:105], v[2:3], 0, s[2:3]
	v_or_b32_e32 v2, s5, v114
	v_ashrrev_i32_e32 v3, 31, v2
	v_lshlrev_b64 v[2:3], 11, v[2:3]
	v_lshl_add_u64 v[106:107], v[104:105], 0, v[2:3]
	v_or_b32_e32 v2, 0x200, v0
	v_lshrrev_b32_e32 v115, 2, v2
	v_or_b32_e32 v2, s5, v115
	v_ashrrev_i32_e32 v3, 31, v2
	s_mul_i32 s4, s4, 10
	v_lshlrev_b64 v[2:3], 11, v[2:3]
	s_sub_i32 s2, s97, s4
	v_lshl_add_u64 v[108:109], v[104:105], 0, v[2:3]
	v_lshl_or_b32 v2, s2, 7, v114
	v_ashrrev_i32_e32 v3, 31, v2
	v_lshlrev_b64 v[2:3], 11, v[2:3]
	v_lshl_add_u64 v[2:3], s[0:1], 0, v[2:3]
	v_lshl_add_u64 v[110:111], v[2:3], 0, v[102:103]
	global_load_dwordx4 v[78:81], v[108:109], off
	global_load_dwordx4 v[90:93], v[108:109], off offset:64
	global_load_dwordx4 v[82:85], v[110:111], off
	global_load_dwordx4 v[94:97], v[110:111], off offset:64
	global_load_dwordx4 v[98:101], v[106:107], off offset:64
	global_load_dwordx4 v[66:69], v[106:107], off offset:128
	global_load_dwordx4 v[74:77], v[108:109], off offset:128
	global_load_dwordx4 v[86:89], v[106:107], off
	global_load_dwordx4 v[70:73], v[110:111], off offset:128
	v_mad_u32_u24 v3, v115, 40, v4
	v_mul_u32_u24_e32 v2, 40, v114
	v_lshl_add_u32 v117, v3, 1, 0
	v_lshrrev_b32_e32 v3, 1, v0
	v_add_lshl_u32 v2, v2, v4, 1
	v_and_b32_e32 v3, 0xc0, v3
	v_and_b32_e32 v4, 31, v0
	v_or_b32_e32 v5, v3, v4
	v_and_b32_e32 v6, 8, v114
	v_mul_u32_u24_e32 v5, 40, v5
	v_lshl_add_u32 v7, v6, 1, 0
	v_lshl_add_u32 v119, v5, 1, v7
	v_and_b32_e32 v5, 0x5f, v0
	v_mov_b32_e32 v11, 0x500
	v_mul_u32_u24_e32 v8, 0x50, v5
	v_mul_u32_u24_e32 v9, 40, v5
	v_mad_u32_u24 v5, v5, 40, v11
	v_add_lshl_u32 v10, v9, v6, 1
	v_add_lshl_u32 v11, v5, v6, 1
	v_or_b32_e32 v6, 16, v6
	s_add_i32 s2, 0, 0x11810
	v_add_lshl_u32 v12, v6, v9, 1
	v_add_lshl_u32 v5, v5, v6, 1
	v_add_u32_e32 v118, s2, v2
	v_add_u32_e32 v120, s2, v10
	v_add_u32_e32 v121, s2, v11
	v_add_u32_e32 v122, s2, v12
	v_add_u32_e32 v123, s2, v5
	s_add_i32 s2, 0, 0x14010
	v_add_u32_e32 v128, s2, v5
	v_lshrrev_b32_e32 v5, 3, v0
	v_add_u32_e32 v116, 0, v2
	v_add_u32_e32 v124, s2, v2
	v_and_b32_e32 v2, 64, v0
	v_and_or_b32 v3, v5, 4, v3
	v_lshl_add_u32 v2, v2, 2, 0
	v_lshlrev_b32_e32 v4, 2, v4
	v_mul_u32_u24_e32 v3, 0x210, v3
	s_waitcnt vmcnt(9)
	v_add3_u32 v131, v2, v4, v3
	v_and_b32_e32 v2, 15, v0
	v_lshl_add_u64 v[112:113], s[0:1], 0, v[102:103]
	s_movk_i32 s0, 0x210
	v_lshrrev_b32_e32 v133, 4, v0
	v_lshlrev_b32_e32 v2, 5, v2
	v_mad_u32_u24 v2, v133, s0, v2
	v_add_u32_e32 v125, s2, v10
	v_add_u32_e32 v126, s2, v11
	v_add_u32_e32 v127, s2, v12
	v_lshl_add_u32 v129, v9, 1, v7
	v_add_u32_e32 v130, 0, v12
	v_or_b32_e32 v132, 0xfffffe00, v0
	v_add3_u32 v134, v2, 0, 16
	v_add_u32_e32 v135, v7, v8
	s_movk_i32 s10, 0x4100
	s_movk_i32 s11, 0xa00
	s_movk_i32 s12, 0xdff
	s_mov_b32 s2, s97
	s_branch .LBB0_1742

; #define G_LOAD(SA, SB, KT) do { SA.load(al, (KT) * 32); SB.load(bl, (KT) * 32); } while (0)
; #define G_STORE(SA, SB, BUF) do { SA.store(As + (BUF) * ASZ, tid); SB.store(Bs3 + (BUF) * BSZ, tid); } while (0)
;     __device__ __forceinline__ void mainloop(bfr* smem, const AL& al, const BL& bl) {
;     ...
;         __syncthreads();
;         G_STORE(sa0, sb0, 0);
;         if (1 < nk) G_STORE(sa1, sb1, 1);
;         if (BL::DEPTH < nk) G_LOAD(sa0, sb0, BL::DEPTH);
;         if (BL::DEPTH + 1 < nk) G_LOAD(sa1, sb1, BL::DEPTH + 1);
;         __builtin_amdgcn_sched_barrier(0);
;         __syncthreads();
;         G_RD(fa0, fb0, 0);
;         if constexpr (BL::DEPTH == 3) {
; #pragma unroll
;             for (int kt = 0; kt < nk; kt += 6) {
;                 G_STEP(0, fa0, fb0, fa1, fb1, 1, sa2, sb2, 2, 3);
;                 G_STEP(1, fa1, fb1, fa0, fb0, 2, sa0, sb0, 0, 3);
;                 G_STEP(2, fa0, fb0, fa1, fb1, 0, sa1, sb1, 1, 3);
;                 G_STEP(3, fa1, fb1, fa0, fb0, 1, sa2, sb2, 2, 3);
;                 G_STEP(4, fa0, fb0, fa1, fb1, 2, sa0, sb0, 0, 3);
;                 G_STEP(5, fa1, fb1, fa0, fb0, 0, sa1, sb1, 1, 3);
.LBB0_1742:
	s_barrier
	global_load_dwordx4 v[136:139], v[106:107], off offset:192
	global_load_dwordx4 v[140:143], v[106:107], off offset:256
	global_load_dwordx4 v[144:147], v[108:109], off offset:192
	global_load_dwordx4 v[148:151], v[108:109], off offset:256
	global_load_dwordx4 v[152:155], v[110:111], off offset:192
	global_load_dwordx4 v[156:159], v[110:111], off offset:256
	s_waitcnt vmcnt(7)
	ds_write_b128 v116, v[86:89] offset:16
	ds_write_b128 v117, v[78:81] offset:16
	ds_write_b128 v116, v[82:85] offset:61456
	ds_write_b128 v116, v[98:101] offset:20496
	ds_write_b128 v117, v[90:93] offset:20496
	ds_write_b128 v118, v[94:97]
	s_waitcnt lgkmcnt(0)
	s_barrier
	ds_read_b128 v[2:5], v119 offset:16
	ds_read_b128 v[78:81], v119 offset:48
	ds_read_b128 v[6:9], v135 offset:61456
	ds_read_b128 v[18:21], v119 offset:2576
	ds_read_b128 v[82:85], v119 offset:2608
	ds_read_b128 v[86:89], v135 offset:61488
	ds_read_b128 v[22:25], v135 offset:64016
	ds_read_b128 v[90:93], v135 offset:64048
	s_waitcnt lgkmcnt(5)
	v_mfma_f32_32x32x16_bf16 v[34:49], v[2:5], v[6:9], 0
	ds_read_b128 v[94:97], v119 offset:20496
	ds_read_b128 v[98:101], v120
	s_waitcnt lgkmcnt(3)
	v_mfma_f32_32x32x16_bf16 v[50:65], v[2:5], v[22:25], 0
	ds_read_b128 v[160:163], v119 offset:23056
	ds_read_b128 v[164:167], v121
	v_mfma_f32_32x32x16_bf16 v[2:17], v[18:21], v[6:9], 0
	ds_read_b128 v[168:171], v119 offset:20528
	ds_read_b128 v[172:175], v122
	v_mfma_f32_32x32x16_bf16 v[18:33], v[18:21], v[22:25], 0
	ds_read_b128 v[176:179], v119 offset:23088
	ds_read_b128 v[180:183], v123
	v_mfma_f32_32x32x16_bf16 v[34:49], v[78:81], v[86:89], v[34:49]
	ds_write_b128 v116, v[66:69] offset:40976
	ds_write_b128 v117, v[74:77] offset:40976
	s_waitcnt lgkmcnt(10)
	v_mfma_f32_32x32x16_bf16 v[50:65], v[78:81], v[90:93], v[50:65]
	s_waitcnt vmcnt(6)
	ds_write_b128 v124, v[70:73]
	v_mfma_f32_32x32x16_bf16 v[2:17], v[82:85], v[86:89], v[2:17]
	global_load_dwordx4 v[66:69], v[106:107], off offset:320
	global_load_dwordx4 v[70:73], v[108:109], off offset:320
	global_load_dwordx4 v[74:77], v[110:111], off offset:320
	v_mfma_f32_32x32x16_bf16 v[18:33], v[82:85], v[90:93], v[18:33]
	s_waitcnt lgkmcnt(0)
	s_barrier
	v_mfma_f32_32x32x16_bf16 v[34:49], v[94:97], v[98:101], v[34:49]
	ds_read_b128 v[78:81], v119 offset:40976
	ds_read_b128 v[82:85], v125
	v_mfma_f32_32x32x16_bf16 v[50:65], v[94:97], v[164:167], v[50:65]
	ds_read_b128 v[86:89], v119 offset:43536
	ds_read_b128 v[90:93], v126
	v_mfma_f32_32x32x16_bf16 v[2:17], v[160:163], v[98:101], v[2:17]
	ds_read_b128 v[94:97], v119 offset:41008
	ds_read_b128 v[98:101], v127
	v_mfma_f32_32x32x16_bf16 v[18:33], v[160:163], v[164:167], v[18:33]
	ds_read_b128 v[160:163], v119 offset:43568
	ds_read_b128 v[164:167], v128
	v_mfma_f32_32x32x16_bf16 v[34:49], v[168:171], v[172:175], v[34:49]
	s_waitcnt vmcnt(8)
	ds_write_b128 v116, v[136:139] offset:16
	s_waitcnt vmcnt(6)
	ds_write_b128 v117, v[144:147] offset:16
	v_mfma_f32_32x32x16_bf16 v[50:65], v[168:171], v[180:183], v[50:65]
	s_waitcnt vmcnt(4)
	ds_write_b128 v116, v[152:155] offset:61456
	v_mfma_f32_32x32x16_bf16 v[2:17], v[176:179], v[172:175], v[2:17]
	global_load_dwordx4 v[136:139], v[106:107], off offset:384
	global_load_dwordx4 v[144:147], v[108:109], off offset:384
	global_load_dwordx4 v[152:155], v[110:111], off offset:384
	v_mfma_f32_32x32x16_bf16 v[18:33], v[176:179], v[180:183], v[18:33]
	s_waitcnt lgkmcnt(0)
	s_barrier
	v_mfma_f32_32x32x16_bf16 v[34:49], v[78:81], v[82:85], v[34:49]
	ds_read_b128 v[168:171], v119 offset:16
	ds_read_b128 v[172:175], v129 offset:61456
	v_mfma_f32_32x32x16_bf16 v[50:65], v[78:81], v[90:93], v[50:65]
	ds_read_b128 v[78:81], v119 offset:2576
	ds_read_b128 v[176:179], v129 offset:64016
	v_mfma_f32_32x32x16_bf16 v[2:17], v[86:89], v[82:85], v[2:17]
	ds_read_b128 v[82:85], v119 offset:48
	ds_read_b128 v[180:183], v129 offset:61488
	v_mfma_f32_32x32x16_bf16 v[18:33], v[86:89], v[90:93], v[18:33]
	ds_read_b128 v[86:89], v119 offset:2608
	ds_read_b128 v[90:93], v130 offset:64016
	v_mfma_f32_32x32x16_bf16 v[34:49], v[94:97], v[98:101], v[34:49]
	ds_write_b128 v116, v[140:143] offset:20496
	ds_write_b128 v117, v[148:151] offset:20496
	v_mfma_f32_32x32x16_bf16 v[50:65], v[94:97], v[164:167], v[50:65]
	s_waitcnt vmcnt(6)
	ds_write_b128 v118, v[156:159]
	v_mfma_f32_32x32x16_bf16 v[2:17], v[160:163], v[98:101], v[2:17]
	global_load_dwordx4 v[94:97], v[106:107], off offset:448
	global_load_dwordx4 v[98:101], v[108:109], off offset:448
	global_load_dwordx4 v[140:143], v[110:111], off offset:448
	v_mfma_f32_32x32x16_bf16 v[18:33], v[160:163], v[164:167], v[18:33]
	s_waitcnt lgkmcnt(0)
	s_barrier
	v_mfma_f32_32x32x16_bf16 v[34:49], v[168:171], v[172:175], v[34:49]
	ds_read_b128 v[148:151], v119 offset:20496
	ds_read_b128 v[156:159], v120
	v_mfma_f32_32x32x16_bf16 v[50:65], v[168:171], v[176:179], v[50:65]
	ds_read_b128 v[160:163], v119 offset:23056
	ds_read_b128 v[164:167], v121
	v_mfma_f32_32x32x16_bf16 v[2:17], v[78:81], v[172:175], v[2:17]
	ds_read_b128 v[168:171], v119 offset:20528
	ds_read_b128 v[172:175], v122
	v_mfma_f32_32x32x16_bf16 v[18:33], v[78:81], v[176:179], v[18:33]
	ds_read_b128 v[78:81], v119 offset:23088
	ds_read_b128 v[176:179], v123
	v_mfma_f32_32x32x16_bf16 v[34:49], v[82:85], v[180:183], v[34:49]
	s_waitcnt vmcnt(8)
	ds_write_b128 v116, v[66:69] offset:40976
	s_waitcnt vmcnt(7)
	ds_write_b128 v117, v[70:73] offset:40976
	v_mfma_f32_32x32x16_bf16 v[50:65], v[82:85], v[90:93], v[50:65]
	s_waitcnt vmcnt(6)
	ds_write_b128 v124, v[74:77]
	v_mfma_f32_32x32x16_bf16 v[2:17], v[86:89], v[180:183], v[2:17]
	global_load_dwordx4 v[66:69], v[106:107], off offset:512
	global_load_dwordx4 v[70:73], v[108:109], off offset:512
	global_load_dwordx4 v[74:77], v[110:111], off offset:512
	v_mfma_f32_32x32x16_bf16 v[18:33], v[86:89], v[90:93], v[18:33]
	s_waitcnt lgkmcnt(0)
	s_barrier
	v_mfma_f32_32x32x16_bf16 v[34:49], v[148:151], v[156:159], v[34:49]
	ds_read_b128 v[82:85], v119 offset:40976
	ds_read_b128 v[86:89], v125
	v_mfma_f32_32x32x16_bf16 v[50:65], v[148:151], v[164:167], v[50:65]
	ds_read_b128 v[90:93], v119 offset:43536
	ds_read_b128 v[148:151], v126
	v_mfma_f32_32x32x16_bf16 v[2:17], v[160:163], v[156:159], v[2:17]
	ds_read_b128 v[156:159], v119 offset:41008
	ds_read_b128 v[180:183], v127
	v_mfma_f32_32x32x16_bf16 v[18:33], v[160:163], v[164:167], v[18:33]
	ds_read_b128 v[160:163], v119 offset:43568
	ds_read_b128 v[164:167], v128
	v_mfma_f32_32x32x16_bf16 v[34:49], v[168:171], v[172:175], v[34:49]
	s_waitcnt vmcnt(8)
	ds_write_b128 v116, v[136:139] offset:16
	s_waitcnt vmcnt(7)
	ds_write_b128 v117, v[144:147] offset:16
	v_mfma_f32_32x32x16_bf16 v[50:65], v[168:171], v[176:179], v[50:65]
	s_waitcnt vmcnt(6)
	ds_write_b128 v116, v[152:155] offset:61456
	v_mfma_f32_32x32x16_bf16 v[2:17], v[78:81], v[172:175], v[2:17]
	global_load_dwordx4 v[136:139], v[106:107], off offset:576
	global_load_dwordx4 v[144:147], v[108:109], off offset:576
	global_load_dwordx4 v[152:155], v[110:111], off offset:576
	v_mfma_f32_32x32x16_bf16 v[18:33], v[78:81], v[176:179], v[18:33]
	s_waitcnt lgkmcnt(0)
	s_barrier
	v_mfma_f32_32x32x16_bf16 v[34:49], v[82:85], v[86:89], v[34:49]
	ds_read_b128 v[78:81], v119 offset:16
	ds_read_b128 v[168:171], v129 offset:61456
	v_mfma_f32_32x32x16_bf16 v[50:65], v[82:85], v[148:151], v[50:65]
	ds_read_b128 v[82:85], v119 offset:2576
	ds_read_b128 v[172:175], v129 offset:64016
	v_mfma_f32_32x32x16_bf16 v[2:17], v[90:93], v[86:89], v[2:17]
	ds_read_b128 v[86:89], v119 offset:48
	ds_read_b128 v[176:179], v129 offset:61488
	v_mfma_f32_32x32x16_bf16 v[18:33], v[90:93], v[148:151], v[18:33]
	ds_read_b128 v[90:93], v119 offset:2608
	ds_read_b128 v[148:151], v130 offset:64016
	v_mfma_f32_32x32x16_bf16 v[34:49], v[156:159], v[180:183], v[34:49]
	s_waitcnt vmcnt(8)
	ds_write_b128 v116, v[94:97] offset:20496
	s_waitcnt vmcnt(7)
	ds_write_b128 v117, v[98:101] offset:20496
	v_mfma_f32_32x32x16_bf16 v[50:65], v[156:159], v[164:167], v[50:65]
	s_waitcnt vmcnt(6)
	ds_write_b128 v118, v[140:143]
	v_mfma_f32_32x32x16_bf16 v[2:17], v[160:163], v[180:183], v[2:17]
	global_load_dwordx4 v[94:97], v[106:107], off offset:640
	global_load_dwordx4 v[98:101], v[108:109], off offset:640
	global_load_dwordx4 v[140:143], v[110:111], off offset:640
	v_mfma_f32_32x32x16_bf16 v[18:33], v[160:163], v[164:167], v[18:33]
	s_waitcnt lgkmcnt(0)
	s_barrier
	v_mfma_f32_32x32x16_bf16 v[34:49], v[78:81], v[168:171], v[34:49]
	ds_read_b128 v[156:159], v119 offset:20496
	ds_read_b128 v[160:163], v120
	v_mfma_f32_32x32x16_bf16 v[50:65], v[78:81], v[172:175], v[50:65]
	ds_read_b128 v[78:81], v119 offset:23056
	ds_read_b128 v[164:167], v121
	v_mfma_f32_32x32x16_bf16 v[2:17], v[82:85], v[168:171], v[2:17]
	ds_read_b128 v[168:171], v119 offset:20528
	ds_read_b128 v[180:183], v122
	v_mfma_f32_32x32x16_bf16 v[18:33], v[82:85], v[172:175], v[18:33]
	ds_read_b128 v[82:85], v119 offset:23088
	ds_read_b128 v[172:175], v123
	v_mfma_f32_32x32x16_bf16 v[34:49], v[86:89], v[176:179], v[34:49]
	s_waitcnt vmcnt(8)
	ds_write_b128 v116, v[66:69] offset:40976
	s_waitcnt vmcnt(7)
	ds_write_b128 v117, v[70:73] offset:40976
	v_mfma_f32_32x32x16_bf16 v[50:65], v[86:89], v[148:151], v[50:65]
	s_waitcnt vmcnt(6)
	ds_write_b128 v124, v[74:77]
	v_mfma_f32_32x32x16_bf16 v[2:17], v[90:93], v[176:179], v[2:17]
	global_load_dwordx4 v[66:69], v[106:107], off offset:704
	global_load_dwordx4 v[70:73], v[108:109], off offset:704
	global_load_dwordx4 v[74:77], v[110:111], off offset:704
	v_mfma_f32_32x32x16_bf16 v[18:33], v[90:93], v[148:151], v[18:33]
	s_waitcnt lgkmcnt(0)
	s_barrier
	v_mfma_f32_32x32x16_bf16 v[34:49], v[156:159], v[160:163], v[34:49]
	ds_read_b128 v[86:89], v119 offset:40976
	ds_read_b128 v[90:93], v125
	v_mfma_f32_32x32x16_bf16 v[50:65], v[156:159], v[164:167], v[50:65]
	ds_read_b128 v[148:151], v119 offset:43536
	ds_read_b128 v[156:159], v126
	v_mfma_f32_32x32x16_bf16 v[2:17], v[78:81], v[160:163], v[2:17]
	ds_read_b128 v[160:163], v119 offset:41008
	ds_read_b128 v[176:179], v127
	v_mfma_f32_32x32x16_bf16 v[18:33], v[78:81], v[164:167], v[18:33]
	ds_read_b128 v[78:81], v119 offset:43568
	ds_read_b128 v[164:167], v128
	v_mfma_f32_32x32x16_bf16 v[34:49], v[168:171], v[180:183], v[34:49]
	s_waitcnt vmcnt(8)
	ds_write_b128 v116, v[136:139] offset:16
	s_waitcnt vmcnt(7)
	ds_write_b128 v117, v[144:147] offset:16
	v_mfma_f32_32x32x16_bf16 v[50:65], v[168:171], v[172:175], v[50:65]
	s_waitcnt vmcnt(6)
	ds_write_b128 v116, v[152:155] offset:61456
	v_mfma_f32_32x32x16_bf16 v[2:17], v[82:85], v[180:183], v[2:17]
	global_load_dwordx4 v[136:139], v[106:107], off offset:768
	global_load_dwordx4 v[144:147], v[108:109], off offset:768
	global_load_dwordx4 v[152:155], v[110:111], off offset:768
	v_mfma_f32_32x32x16_bf16 v[18:33], v[82:85], v[172:175], v[18:33]
	s_waitcnt lgkmcnt(0)
	s_barrier
	v_mfma_f32_32x32x16_bf16 v[34:49], v[86:89], v[90:93], v[34:49]
	ds_read_b128 v[82:85], v119 offset:16
	ds_read_b128 v[168:171], v129 offset:61456
	v_mfma_f32_32x32x16_bf16 v[50:65], v[86:89], v[156:159], v[50:65]
	ds_read_b128 v[86:89], v119 offset:2576
	ds_read_b128 v[172:175], v129 offset:64016
	v_mfma_f32_32x32x16_bf16 v[2:17], v[148:151], v[90:93], v[2:17]
	ds_read_b128 v[90:93], v119 offset:48
	ds_read_b128 v[180:183], v129 offset:61488
	v_mfma_f32_32x32x16_bf16 v[18:33], v[148:151], v[156:159], v[18:33]
	ds_read_b128 v[148:151], v119 offset:2608
	ds_read_b128 v[156:159], v130 offset:64016
	v_mfma_f32_32x32x16_bf16 v[34:49], v[160:163], v[176:179], v[34:49]
	s_waitcnt vmcnt(8)
	ds_write_b128 v116, v[94:97] offset:20496
	s_waitcnt vmcnt(7)
	ds_write_b128 v117, v[98:101] offset:20496
	v_mfma_f32_32x32x16_bf16 v[50:65], v[160:163], v[164:167], v[50:65]
	s_waitcnt vmcnt(6)
	ds_write_b128 v118, v[140:143]
	v_mfma_f32_32x32x16_bf16 v[2:17], v[78:81], v[176:179], v[2:17]
	global_load_dwordx4 v[94:97], v[106:107], off offset:832
	global_load_dwordx4 v[98:101], v[108:109], off offset:832
	global_load_dwordx4 v[140:143], v[110:111], off offset:832
	v_mfma_f32_32x32x16_bf16 v[18:33], v[78:81], v[164:167], v[18:33]
	s_waitcnt lgkmcnt(0)
	s_barrier
	v_mfma_f32_32x32x16_bf16 v[34:49], v[82:85], v[168:171], v[34:49]
	ds_read_b128 v[78:81], v119 offset:20496
	ds_read_b128 v[160:163], v120
	v_mfma_f32_32x32x16_bf16 v[50:65], v[82:85], v[172:175], v[50:65]
	ds_read_b128 v[82:85], v119 offset:23056
	ds_read_b128 v[164:167], v121
	v_mfma_f32_32x32x16_bf16 v[2:17], v[86:89], v[168:171], v[2:17]
	ds_read_b128 v[168:171], v119 offset:20528
	ds_read_b128 v[176:179], v122
	v_mfma_f32_32x32x16_bf16 v[18:33], v[86:89], v[172:175], v[18:33]
	ds_read_b128 v[86:89], v119 offset:23088
	ds_read_b128 v[172:175], v123
	v_mfma_f32_32x32x16_bf16 v[34:49], v[90:93], v[180:183], v[34:49]
	s_waitcnt vmcnt(8)
	ds_write_b128 v116, v[66:69] offset:40976
	s_waitcnt vmcnt(7)
	ds_write_b128 v117, v[70:73] offset:40976
	v_mfma_f32_32x32x16_bf16 v[50:65], v[90:93], v[156:159], v[50:65]
	s_waitcnt vmcnt(6)
	ds_write_b128 v124, v[74:77]
	v_mfma_f32_32x32x16_bf16 v[2:17], v[148:151], v[180:183], v[2:17]
	global_load_dwordx4 v[66:69], v[106:107], off offset:896
	global_load_dwordx4 v[70:73], v[108:109], off offset:896
	global_load_dwordx4 v[74:77], v[110:111], off offset:896
	v_mfma_f32_32x32x16_bf16 v[18:33], v[148:151], v[156:159], v[18:33]
	s_waitcnt lgkmcnt(0)
	s_barrier
	v_mfma_f32_32x32x16_bf16 v[34:49], v[78:81], v[160:163], v[34:49]
	ds_read_b128 v[90:93], v119 offset:40976
	ds_read_b128 v[148:151], v125
	v_mfma_f32_32x32x16_bf16 v[50:65], v[78:81], v[164:167], v[50:65]
	ds_read_b128 v[78:81], v119 offset:43536
	ds_read_b128 v[156:159], v126
	v_mfma_f32_32x32x16_bf16 v[2:17], v[82:85], v[160:163], v[2:17]
	ds_read_b128 v[160:163], v119 offset:41008
	ds_read_b128 v[180:183], v127
	v_mfma_f32_32x32x16_bf16 v[18:33], v[82:85], v[164:167], v[18:33]
	ds_read_b128 v[82:85], v119 offset:43568
	ds_read_b128 v[164:167], v128
	v_mfma_f32_32x32x16_bf16 v[34:49], v[168:171], v[176:179], v[34:49]
	s_waitcnt vmcnt(8)
	ds_write_b128 v116, v[136:139] offset:16
	s_waitcnt vmcnt(7)
	ds_write_b128 v117, v[144:147] offset:16
	v_mfma_f32_32x32x16_bf16 v[50:65], v[168:171], v[172:175], v[50:65]
	s_waitcnt vmcnt(6)
	ds_write_b128 v116, v[152:155] offset:61456
	v_mfma_f32_32x32x16_bf16 v[2:17], v[86:89], v[176:179], v[2:17]
	global_load_dwordx4 v[136:139], v[106:107], off offset:960
	global_load_dwordx4 v[144:147], v[108:109], off offset:960
	global_load_dwordx4 v[152:155], v[110:111], off offset:960
	v_mfma_f32_32x32x16_bf16 v[18:33], v[86:89], v[172:175], v[18:33]
	s_waitcnt lgkmcnt(0)
	s_barrier
	v_mfma_f32_32x32x16_bf16 v[34:49], v[90:93], v[148:151], v[34:49]
	ds_read_b128 v[86:89], v119 offset:16
	ds_read_b128 v[168:171], v129 offset:61456
	v_mfma_f32_32x32x16_bf16 v[50:65], v[90:93], v[156:159], v[50:65]
	ds_read_b128 v[90:93], v119 offset:2576
	ds_read_b128 v[172:175], v129 offset:64016
	v_mfma_f32_32x32x16_bf16 v[2:17], v[78:81], v[148:151], v[2:17]
	ds_read_b128 v[148:151], v119 offset:48
	ds_read_b128 v[176:179], v129 offset:61488
	v_mfma_f32_32x32x16_bf16 v[18:33], v[78:81], v[156:159], v[18:33]
	ds_read_b128 v[78:81], v119 offset:2608
	ds_read_b128 v[156:159], v130 offset:64016
	v_mfma_f32_32x32x16_bf16 v[34:49], v[160:163], v[180:183], v[34:49]
	s_waitcnt vmcnt(8)
	ds_write_b128 v116, v[94:97] offset:20496
	s_waitcnt vmcnt(7)
	ds_write_b128 v117, v[98:101] offset:20496
	v_mfma_f32_32x32x16_bf16 v[50:65], v[160:163], v[164:167], v[50:65]
	s_waitcnt vmcnt(6)
	ds_write_b128 v118, v[140:143]
	v_mfma_f32_32x32x16_bf16 v[2:17], v[82:85], v[180:183], v[2:17]
	global_load_dwordx4 v[94:97], v[106:107], off offset:1024
	global_load_dwordx4 v[98:101], v[108:109], off offset:1024
	global_load_dwordx4 v[140:143], v[110:111], off offset:1024
	v_mfma_f32_32x32x16_bf16 v[18:33], v[82:85], v[164:167], v[18:33]
	s_waitcnt lgkmcnt(0)
	s_barrier
	v_mfma_f32_32x32x16_bf16 v[34:49], v[86:89], v[168:171], v[34:49]
	ds_read_b128 v[82:85], v119 offset:20496
	ds_read_b128 v[160:163], v120
	v_mfma_f32_32x32x16_bf16 v[50:65], v[86:89], v[172:175], v[50:65]
	ds_read_b128 v[86:89], v119 offset:23056
	ds_read_b128 v[164:167], v121
	v_mfma_f32_32x32x16_bf16 v[2:17], v[90:93], v[168:171], v[2:17]
	ds_read_b128 v[168:171], v119 offset:20528
	ds_read_b128 v[180:183], v122
	v_mfma_f32_32x32x16_bf16 v[18:33], v[90:93], v[172:175], v[18:33]
	ds_read_b128 v[90:93], v119 offset:23088
	ds_read_b128 v[172:175], v123
	v_mfma_f32_32x32x16_bf16 v[34:49], v[148:151], v[176:179], v[34:49]
	s_waitcnt vmcnt(8)
	ds_write_b128 v116, v[66:69] offset:40976
	s_waitcnt vmcnt(7)
	ds_write_b128 v117, v[70:73] offset:40976
	v_mfma_f32_32x32x16_bf16 v[50:65], v[148:151], v[156:159], v[50:65]
	s_waitcnt vmcnt(6)
	ds_write_b128 v124, v[74:77]
	v_mfma_f32_32x32x16_bf16 v[2:17], v[78:81], v[176:179], v[2:17]
	global_load_dwordx4 v[66:69], v[106:107], off offset:1088
	global_load_dwordx4 v[70:73], v[108:109], off offset:1088
	global_load_dwordx4 v[74:77], v[110:111], off offset:1088
	v_mfma_f32_32x32x16_bf16 v[18:33], v[78:81], v[156:159], v[18:33]
	s_waitcnt lgkmcnt(0)
	s_barrier
	v_mfma_f32_32x32x16_bf16 v[34:49], v[82:85], v[160:163], v[34:49]
	ds_read_b128 v[78:81], v119 offset:40976
	ds_read_b128 v[148:151], v125
	v_mfma_f32_32x32x16_bf16 v[50:65], v[82:85], v[164:167], v[50:65]
	ds_read_b128 v[82:85], v119 offset:43536
	ds_read_b128 v[156:159], v126
	v_mfma_f32_32x32x16_bf16 v[2:17], v[86:89], v[160:163], v[2:17]
	ds_read_b128 v[160:163], v119 offset:41008
	ds_read_b128 v[176:179], v127
	v_mfma_f32_32x32x16_bf16 v[18:33], v[86:89], v[164:167], v[18:33]
	ds_read_b128 v[86:89], v119 offset:43568
	ds_read_b128 v[164:167], v128
	v_mfma_f32_32x32x16_bf16 v[34:49], v[168:171], v[180:183], v[34:49]
	s_waitcnt vmcnt(8)
	ds_write_b128 v116, v[136:139] offset:16
	s_waitcnt vmcnt(7)
	ds_write_b128 v117, v[144:147] offset:16
	v_mfma_f32_32x32x16_bf16 v[50:65], v[168:171], v[172:175], v[50:65]
	s_waitcnt vmcnt(6)
	ds_write_b128 v116, v[152:155] offset:61456
	v_mfma_f32_32x32x16_bf16 v[2:17], v[90:93], v[180:183], v[2:17]
	global_load_dwordx4 v[136:139], v[106:107], off offset:1152
	global_load_dwordx4 v[144:147], v[108:109], off offset:1152
	global_load_dwordx4 v[152:155], v[110:111], off offset:1152
	v_mfma_f32_32x32x16_bf16 v[18:33], v[90:93], v[172:175], v[18:33]
	s_waitcnt lgkmcnt(0)
	s_barrier
	v_mfma_f32_32x32x16_bf16 v[34:49], v[78:81], v[148:151], v[34:49]
	ds_read_b128 v[90:93], v119 offset:16
	ds_read_b128 v[168:171], v129 offset:61456
	v_mfma_f32_32x32x16_bf16 v[50:65], v[78:81], v[156:159], v[50:65]
	ds_read_b128 v[78:81], v119 offset:2576
	ds_read_b128 v[172:175], v129 offset:64016
	v_mfma_f32_32x32x16_bf16 v[2:17], v[82:85], v[148:151], v[2:17]
	ds_read_b128 v[148:151], v119 offset:48
	ds_read_b128 v[180:183], v129 offset:61488
	v_mfma_f32_32x32x16_bf16 v[18:33], v[82:85], v[156:159], v[18:33]
	ds_read_b128 v[82:85], v119 offset:2608
	ds_read_b128 v[156:159], v130 offset:64016
	v_mfma_f32_32x32x16_bf16 v[34:49], v[160:163], v[176:179], v[34:49]
	s_waitcnt vmcnt(8)
	ds_write_b128 v116, v[94:97] offset:20496
	s_waitcnt vmcnt(7)
	ds_write_b128 v117, v[98:101] offset:20496
	v_mfma_f32_32x32x16_bf16 v[50:65], v[160:163], v[164:167], v[50:65]
	s_waitcnt vmcnt(6)
	ds_write_b128 v118, v[140:143]
	v_mfma_f32_32x32x16_bf16 v[2:17], v[86:89], v[176:179], v[2:17]
	global_load_dwordx4 v[94:97], v[106:107], off offset:1216
	global_load_dwordx4 v[98:101], v[108:109], off offset:1216
	global_load_dwordx4 v[140:143], v[110:111], off offset:1216
	v_mfma_f32_32x32x16_bf16 v[18:33], v[86:89], v[164:167], v[18:33]
	s_waitcnt lgkmcnt(0)
	s_barrier
	v_mfma_f32_32x32x16_bf16 v[34:49], v[90:93], v[168:171], v[34:49]
	ds_read_b128 v[86:89], v119 offset:20496
	ds_read_b128 v[160:163], v120
	v_mfma_f32_32x32x16_bf16 v[50:65], v[90:93], v[172:175], v[50:65]
	ds_read_b128 v[90:93], v119 offset:23056
	ds_read_b128 v[164:167], v121
	v_mfma_f32_32x32x16_bf16 v[2:17], v[78:81], v[168:171], v[2:17]
	ds_read_b128 v[168:171], v119 offset:20528
	ds_read_b128 v[176:179], v122
	v_mfma_f32_32x32x16_bf16 v[18:33], v[78:81], v[172:175], v[18:33]
	ds_read_b128 v[78:81], v119 offset:23088
	ds_read_b128 v[172:175], v123
	v_mfma_f32_32x32x16_bf16 v[34:49], v[148:151], v[180:183], v[34:49]
	s_waitcnt vmcnt(8)
	ds_write_b128 v116, v[66:69] offset:40976
	s_waitcnt vmcnt(7)
	ds_write_b128 v117, v[70:73] offset:40976
	v_mfma_f32_32x32x16_bf16 v[50:65], v[148:151], v[156:159], v[50:65]
	s_waitcnt vmcnt(6)
	ds_write_b128 v124, v[74:77]
	v_mfma_f32_32x32x16_bf16 v[2:17], v[82:85], v[180:183], v[2:17]
	global_load_dwordx4 v[66:69], v[106:107], off offset:1280
	global_load_dwordx4 v[70:73], v[108:109], off offset:1280
	global_load_dwordx4 v[74:77], v[110:111], off offset:1280
	v_mfma_f32_32x32x16_bf16 v[18:33], v[82:85], v[156:159], v[18:33]
	s_waitcnt lgkmcnt(0)
	s_barrier
	v_mfma_f32_32x32x16_bf16 v[34:49], v[86:89], v[160:163], v[34:49]
	ds_read_b128 v[82:85], v119 offset:40976
	ds_read_b128 v[148:151], v125
	v_mfma_f32_32x32x16_bf16 v[50:65], v[86:89], v[164:167], v[50:65]
	ds_read_b128 v[86:89], v119 offset:43536
	ds_read_b128 v[156:159], v126
	v_mfma_f32_32x32x16_bf16 v[2:17], v[90:93], v[160:163], v[2:17]
	ds_read_b128 v[160:163], v119 offset:41008
	ds_read_b128 v[180:183], v127
	v_mfma_f32_32x32x16_bf16 v[18:33], v[90:93], v[164:167], v[18:33]
	ds_read_b128 v[90:93], v119 offset:43568
	ds_read_b128 v[164:167], v128
	v_mfma_f32_32x32x16_bf16 v[34:49], v[168:171], v[176:179], v[34:49]
	s_waitcnt vmcnt(8)
	ds_write_b128 v116, v[136:139] offset:16
	s_waitcnt vmcnt(7)
	ds_write_b128 v117, v[144:147] offset:16
	v_mfma_f32_32x32x16_bf16 v[50:65], v[168:171], v[172:175], v[50:65]
	s_waitcnt vmcnt(6)
	ds_write_b128 v116, v[152:155] offset:61456
	v_mfma_f32_32x32x16_bf16 v[2:17], v[78:81], v[176:179], v[2:17]
	global_load_dwordx4 v[136:139], v[106:107], off offset:1344
	global_load_dwordx4 v[144:147], v[108:109], off offset:1344
	global_load_dwordx4 v[152:155], v[110:111], off offset:1344
	v_mfma_f32_32x32x16_bf16 v[18:33], v[78:81], v[172:175], v[18:33]
	s_waitcnt lgkmcnt(0)
	s_barrier
	v_mfma_f32_32x32x16_bf16 v[34:49], v[82:85], v[148:151], v[34:49]
	ds_read_b128 v[78:81], v119 offset:16
	ds_read_b128 v[168:171], v129 offset:61456
	v_mfma_f32_32x32x16_bf16 v[50:65], v[82:85], v[156:159], v[50:65]
	ds_read_b128 v[82:85], v119 offset:2576
	ds_read_b128 v[172:175], v129 offset:64016
	v_mfma_f32_32x32x16_bf16 v[2:17], v[86:89], v[148:151], v[2:17]
	ds_read_b128 v[148:151], v119 offset:48
	ds_read_b128 v[176:179], v129 offset:61488
	v_mfma_f32_32x32x16_bf16 v[18:33], v[86:89], v[156:159], v[18:33]
	ds_read_b128 v[86:89], v119 offset:2608
	ds_read_b128 v[156:159], v130 offset:64016
	v_mfma_f32_32x32x16_bf16 v[34:49], v[160:163], v[180:183], v[34:49]
	s_waitcnt vmcnt(8)
	ds_write_b128 v116, v[94:97] offset:20496
	s_waitcnt vmcnt(7)
	ds_write_b128 v117, v[98:101] offset:20496
	v_mfma_f32_32x32x16_bf16 v[50:65], v[160:163], v[164:167], v[50:65]
	s_waitcnt vmcnt(6)
	ds_write_b128 v118, v[140:143]
	v_mfma_f32_32x32x16_bf16 v[2:17], v[90:93], v[180:183], v[2:17]
	global_load_dwordx4 v[94:97], v[106:107], off offset:1408
	global_load_dwordx4 v[98:101], v[108:109], off offset:1408
	global_load_dwordx4 v[140:143], v[110:111], off offset:1408
	v_mfma_f32_32x32x16_bf16 v[18:33], v[90:93], v[164:167], v[18:33]
	s_waitcnt lgkmcnt(0)
	s_barrier
	v_mfma_f32_32x32x16_bf16 v[34:49], v[78:81], v[168:171], v[34:49]
	ds_read_b128 v[90:93], v119 offset:20496
	ds_read_b128 v[160:163], v120
	v_mfma_f32_32x32x16_bf16 v[50:65], v[78:81], v[172:175], v[50:65]
	ds_read_b128 v[78:81], v119 offset:23056
	ds_read_b128 v[164:167], v121
	v_mfma_f32_32x32x16_bf16 v[2:17], v[82:85], v[168:171], v[2:17]
	ds_read_b128 v[168:171], v119 offset:20528
	ds_read_b128 v[180:183], v122
	v_mfma_f32_32x32x16_bf16 v[18:33], v[82:85], v[172:175], v[18:33]
	ds_read_b128 v[82:85], v119 offset:23088
	ds_read_b128 v[172:175], v123
	v_mfma_f32_32x32x16_bf16 v[34:49], v[148:151], v[176:179], v[34:49]
	s_waitcnt vmcnt(8)
	ds_write_b128 v116, v[66:69] offset:40976
	s_waitcnt vmcnt(7)
	ds_write_b128 v117, v[70:73] offset:40976
	v_mfma_f32_32x32x16_bf16 v[50:65], v[148:151], v[156:159], v[50:65]
	s_waitcnt vmcnt(6)
	ds_write_b128 v124, v[74:77]
	v_mfma_f32_32x32x16_bf16 v[2:17], v[86:89], v[176:179], v[2:17]
	global_load_dwordx4 v[66:69], v[106:107], off offset:1472
	global_load_dwordx4 v[70:73], v[108:109], off offset:1472
	global_load_dwordx4 v[74:77], v[110:111], off offset:1472
	v_mfma_f32_32x32x16_bf16 v[18:33], v[86:89], v[156:159], v[18:33]
	s_waitcnt lgkmcnt(0)
	s_barrier
	v_mfma_f32_32x32x16_bf16 v[34:49], v[90:93], v[160:163], v[34:49]
	ds_read_b128 v[86:89], v119 offset:40976
	ds_read_b128 v[148:151], v125
	v_mfma_f32_32x32x16_bf16 v[50:65], v[90:93], v[164:167], v[50:65]
	ds_read_b128 v[90:93], v119 offset:43536
	ds_read_b128 v[156:159], v126
	v_mfma_f32_32x32x16_bf16 v[2:17], v[78:81], v[160:163], v[2:17]
	ds_read_b128 v[160:163], v119 offset:41008
	ds_read_b128 v[176:179], v127
	v_mfma_f32_32x32x16_bf16 v[18:33], v[78:81], v[164:167], v[18:33]
	ds_read_b128 v[78:81], v119 offset:43568
	ds_read_b128 v[164:167], v128
	v_mfma_f32_32x32x16_bf16 v[34:49], v[168:171], v[180:183], v[34:49]
	s_waitcnt vmcnt(8)
	ds_write_b128 v116, v[136:139] offset:16
	s_waitcnt vmcnt(7)
	ds_write_b128 v117, v[144:147] offset:16
	v_mfma_f32_32x32x16_bf16 v[50:65], v[168:171], v[172:175], v[50:65]
	s_waitcnt vmcnt(6)
	ds_write_b128 v116, v[152:155] offset:61456
	v_mfma_f32_32x32x16_bf16 v[2:17], v[82:85], v[180:183], v[2:17]
	global_load_dwordx4 v[136:139], v[106:107], off offset:1536
	global_load_dwordx4 v[144:147], v[108:109], off offset:1536
	global_load_dwordx4 v[152:155], v[110:111], off offset:1536
	v_mfma_f32_32x32x16_bf16 v[18:33], v[82:85], v[172:175], v[18:33]
	s_waitcnt lgkmcnt(0)
	s_barrier
	v_mfma_f32_32x32x16_bf16 v[34:49], v[86:89], v[148:151], v[34:49]
	ds_read_b128 v[82:85], v119 offset:16
	ds_read_b128 v[168:171], v129 offset:61456
	v_mfma_f32_32x32x16_bf16 v[50:65], v[86:89], v[156:159], v[50:65]
	ds_read_b128 v[86:89], v119 offset:2576
	ds_read_b128 v[172:175], v129 offset:64016
	v_mfma_f32_32x32x16_bf16 v[2:17], v[90:93], v[148:151], v[2:17]
	ds_read_b128 v[148:151], v119 offset:48
	ds_read_b128 v[180:183], v129 offset:61488
	v_mfma_f32_32x32x16_bf16 v[18:33], v[90:93], v[156:159], v[18:33]
	ds_read_b128 v[90:93], v119 offset:2608
	ds_read_b128 v[156:159], v130 offset:64016
	v_mfma_f32_32x32x16_bf16 v[34:49], v[160:163], v[176:179], v[34:49]
	s_waitcnt vmcnt(8)
	ds_write_b128 v116, v[94:97] offset:20496
	s_waitcnt vmcnt(7)
	ds_write_b128 v117, v[98:101] offset:20496
	v_mfma_f32_32x32x16_bf16 v[50:65], v[160:163], v[164:167], v[50:65]
	s_waitcnt vmcnt(6)
	ds_write_b128 v118, v[140:143]
	v_mfma_f32_32x32x16_bf16 v[2:17], v[78:81], v[176:179], v[2:17]
	global_load_dwordx4 v[94:97], v[106:107], off offset:1600
	global_load_dwordx4 v[98:101], v[108:109], off offset:1600
	global_load_dwordx4 v[140:143], v[110:111], off offset:1600
	v_mfma_f32_32x32x16_bf16 v[18:33], v[78:81], v[164:167], v[18:33]
	s_waitcnt lgkmcnt(0)
	s_barrier
	v_mfma_f32_32x32x16_bf16 v[34:49], v[82:85], v[168:171], v[34:49]
	ds_read_b128 v[78:81], v119 offset:20496
	ds_read_b128 v[160:163], v120
	v_mfma_f32_32x32x16_bf16 v[50:65], v[82:85], v[172:175], v[50:65]
	ds_read_b128 v[82:85], v119 offset:23056
	ds_read_b128 v[164:167], v121
	v_mfma_f32_32x32x16_bf16 v[2:17], v[86:89], v[168:171], v[2:17]
	ds_read_b128 v[168:171], v119 offset:20528
	ds_read_b128 v[176:179], v122
	v_mfma_f32_32x32x16_bf16 v[18:33], v[86:89], v[172:175], v[18:33]
	ds_read_b128 v[86:89], v119 offset:23088
	ds_read_b128 v[172:175], v123
	v_mfma_f32_32x32x16_bf16 v[34:49], v[148:151], v[180:183], v[34:49]
	s_waitcnt vmcnt(8)
	ds_write_b128 v116, v[66:69] offset:40976
	s_waitcnt vmcnt(7)
	ds_write_b128 v117, v[70:73] offset:40976
	v_mfma_f32_32x32x16_bf16 v[50:65], v[148:151], v[156:159], v[50:65]
	s_waitcnt vmcnt(6)
	ds_write_b128 v124, v[74:77]
	v_mfma_f32_32x32x16_bf16 v[2:17], v[90:93], v[180:183], v[2:17]
	global_load_dwordx4 v[66:69], v[106:107], off offset:1664
	global_load_dwordx4 v[70:73], v[108:109], off offset:1664
	global_load_dwordx4 v[74:77], v[110:111], off offset:1664
	v_mfma_f32_32x32x16_bf16 v[18:33], v[90:93], v[156:159], v[18:33]
	s_waitcnt lgkmcnt(0)
	s_barrier
	v_mfma_f32_32x32x16_bf16 v[34:49], v[78:81], v[160:163], v[34:49]
	ds_read_b128 v[90:93], v119 offset:40976
	ds_read_b128 v[148:151], v125
	v_mfma_f32_32x32x16_bf16 v[50:65], v[78:81], v[164:167], v[50:65]
	ds_read_b128 v[78:81], v119 offset:43536
	ds_read_b128 v[156:159], v126
	v_mfma_f32_32x32x16_bf16 v[2:17], v[82:85], v[160:163], v[2:17]
	ds_read_b128 v[160:163], v119 offset:41008
	ds_read_b128 v[180:183], v127
	v_mfma_f32_32x32x16_bf16 v[18:33], v[82:85], v[164:167], v[18:33]
	ds_read_b128 v[82:85], v119 offset:43568
	ds_read_b128 v[164:167], v128
	v_mfma_f32_32x32x16_bf16 v[34:49], v[168:171], v[176:179], v[34:49]
	s_waitcnt vmcnt(8)
	ds_write_b128 v116, v[136:139] offset:16
	s_waitcnt vmcnt(7)
	ds_write_b128 v117, v[144:147] offset:16
	v_mfma_f32_32x32x16_bf16 v[50:65], v[168:171], v[172:175], v[50:65]
	s_waitcnt vmcnt(6)
	ds_write_b128 v116, v[152:155] offset:61456
	v_mfma_f32_32x32x16_bf16 v[2:17], v[86:89], v[176:179], v[2:17]
	global_load_dwordx4 v[136:139], v[106:107], off offset:1728
	global_load_dwordx4 v[144:147], v[108:109], off offset:1728
	global_load_dwordx4 v[152:155], v[110:111], off offset:1728
	v_mfma_f32_32x32x16_bf16 v[18:33], v[86:89], v[172:175], v[18:33]
	s_waitcnt lgkmcnt(0)
	s_barrier
	v_mfma_f32_32x32x16_bf16 v[34:49], v[90:93], v[148:151], v[34:49]
	ds_read_b128 v[86:89], v119 offset:16
	ds_read_b128 v[168:171], v129 offset:61456
	v_mfma_f32_32x32x16_bf16 v[50:65], v[90:93], v[156:159], v[50:65]
	ds_read_b128 v[90:93], v119 offset:2576
	ds_read_b128 v[172:175], v129 offset:64016
	v_mfma_f32_32x32x16_bf16 v[2:17], v[78:81], v[148:151], v[2:17]
	ds_read_b128 v[148:151], v119 offset:48
	ds_read_b128 v[176:179], v129 offset:61488
	v_mfma_f32_32x32x16_bf16 v[18:33], v[78:81], v[156:159], v[18:33]
	ds_read_b128 v[78:81], v119 offset:2608
	ds_read_b128 v[156:159], v130 offset:64016
	v_mfma_f32_32x32x16_bf16 v[34:49], v[160:163], v[180:183], v[34:49]
	s_waitcnt vmcnt(8)
	ds_write_b128 v116, v[94:97] offset:20496
	s_waitcnt vmcnt(7)
	ds_write_b128 v117, v[98:101] offset:20496
	v_mfma_f32_32x32x16_bf16 v[50:65], v[160:163], v[164:167], v[50:65]
	s_waitcnt vmcnt(6)
	ds_write_b128 v118, v[140:143]
	v_mfma_f32_32x32x16_bf16 v[2:17], v[82:85], v[180:183], v[2:17]
	global_load_dwordx4 v[94:97], v[106:107], off offset:1792
	global_load_dwordx4 v[98:101], v[108:109], off offset:1792
	global_load_dwordx4 v[140:143], v[110:111], off offset:1792
	v_mfma_f32_32x32x16_bf16 v[18:33], v[82:85], v[164:167], v[18:33]
	s_waitcnt lgkmcnt(0)
	s_barrier
	v_mfma_f32_32x32x16_bf16 v[34:49], v[86:89], v[168:171], v[34:49]
	ds_read_b128 v[82:85], v119 offset:20496
	ds_read_b128 v[160:163], v120
	v_mfma_f32_32x32x16_bf16 v[50:65], v[86:89], v[172:175], v[50:65]
	ds_read_b128 v[86:89], v119 offset:23056
	ds_read_b128 v[164:167], v121
	v_mfma_f32_32x32x16_bf16 v[2:17], v[90:93], v[168:171], v[2:17]
	ds_read_b128 v[168:171], v119 offset:20528
	ds_read_b128 v[180:183], v122
	v_mfma_f32_32x32x16_bf16 v[18:33], v[90:93], v[172:175], v[18:33]
	ds_read_b128 v[90:93], v119 offset:23088
	ds_read_b128 v[172:175], v123
	v_mfma_f32_32x32x16_bf16 v[34:49], v[148:151], v[176:179], v[34:49]
	s_waitcnt vmcnt(8)
	ds_write_b128 v116, v[66:69] offset:40976
	s_waitcnt vmcnt(7)
	ds_write_b128 v117, v[70:73] offset:40976
	v_mfma_f32_32x32x16_bf16 v[50:65], v[148:151], v[156:159], v[50:65]
	s_waitcnt vmcnt(6)
	ds_write_b128 v124, v[74:77]
	v_mfma_f32_32x32x16_bf16 v[2:17], v[78:81], v[176:179], v[2:17]
	global_load_dwordx4 v[66:69], v[106:107], off offset:1856
	global_load_dwordx4 v[74:77], v[108:109], off offset:1856
	global_load_dwordx4 v[70:73], v[110:111], off offset:1856
	v_mfma_f32_32x32x16_bf16 v[18:33], v[78:81], v[156:159], v[18:33]
	s_waitcnt lgkmcnt(0)
	s_barrier
	v_mfma_f32_32x32x16_bf16 v[34:49], v[82:85], v[160:163], v[34:49]
	ds_read_b128 v[148:151], v119 offset:40976
	ds_read_b128 v[156:159], v125
	v_mfma_f32_32x32x16_bf16 v[50:65], v[82:85], v[164:167], v[50:65]
	ds_read_b128 v[176:179], v119 offset:43536
	ds_read_b128 v[184:187], v126
	v_mfma_f32_32x32x16_bf16 v[2:17], v[86:89], v[160:163], v[2:17]
	ds_read_b128 v[160:163], v119 offset:41008
	ds_read_b128 v[188:191], v127
	v_mfma_f32_32x32x16_bf16 v[18:33], v[86:89], v[164:167], v[18:33]
	ds_read_b128 v[164:167], v119 offset:43568
	ds_read_b128 v[192:195], v128
	v_mfma_f32_32x32x16_bf16 v[34:49], v[168:171], v[180:183], v[34:49]
	s_waitcnt vmcnt(8)
	ds_write_b128 v116, v[136:139] offset:16
	s_waitcnt vmcnt(7)
	ds_write_b128 v117, v[144:147] offset:16
	v_mfma_f32_32x32x16_bf16 v[50:65], v[168:171], v[172:175], v[50:65]
	s_waitcnt vmcnt(6)
	ds_write_b128 v116, v[152:155] offset:61456
	v_mfma_f32_32x32x16_bf16 v[2:17], v[90:93], v[180:183], v[2:17]
	global_load_dwordx4 v[86:89], v[106:107], off offset:1920
	global_load_dwordx4 v[78:81], v[108:109], off offset:1920
	global_load_dwordx4 v[82:85], v[110:111], off offset:1920
	v_mfma_f32_32x32x16_bf16 v[18:33], v[90:93], v[172:175], v[18:33]
	s_waitcnt lgkmcnt(0)
	s_barrier
	v_mfma_f32_32x32x16_bf16 v[34:49], v[148:151], v[156:159], v[34:49]
	ds_read_b128 v[136:139], v119 offset:16
	ds_read_b128 v[144:147], v129 offset:61456
	v_mfma_f32_32x32x16_bf16 v[50:65], v[148:151], v[184:187], v[50:65]
	ds_read_b128 v[148:151], v119 offset:2576
	ds_read_b128 v[152:155], v129 offset:64016
	v_mfma_f32_32x32x16_bf16 v[2:17], v[176:179], v[156:159], v[2:17]
	ds_read_b128 v[156:159], v119 offset:48
	ds_read_b128 v[168:171], v129 offset:61488
	v_mfma_f32_32x32x16_bf16 v[18:33], v[176:179], v[184:187], v[18:33]
	ds_read_b128 v[172:175], v119 offset:2608
	ds_read_b128 v[176:179], v130 offset:64016
	v_mfma_f32_32x32x16_bf16 v[34:49], v[160:163], v[188:191], v[34:49]
	s_waitcnt vmcnt(8)
	ds_write_b128 v116, v[94:97] offset:20496
	s_waitcnt vmcnt(7)
	ds_write_b128 v117, v[98:101] offset:20496
	v_mfma_f32_32x32x16_bf16 v[50:65], v[160:163], v[192:195], v[50:65]
	s_waitcnt vmcnt(6)
	ds_write_b128 v118, v[140:143]
	v_mfma_f32_32x32x16_bf16 v[2:17], v[164:167], v[188:191], v[2:17]
	global_load_dwordx4 v[98:101], v[106:107], off offset:1984
	global_load_dwordx4 v[90:93], v[108:109], off offset:1984
	global_load_dwordx4 v[94:97], v[110:111], off offset:1984
	v_mfma_f32_32x32x16_bf16 v[18:33], v[164:167], v[192:195], v[18:33]
	s_waitcnt lgkmcnt(0)
	s_barrier
	v_mfma_f32_32x32x16_bf16 v[34:49], v[136:139], v[144:147], v[34:49]
	ds_read_b128 v[140:143], v119 offset:20496
	ds_read_b128 v[160:163], v120
	v_mfma_f32_32x32x16_bf16 v[50:65], v[136:139], v[152:155], v[50:65]
	ds_read_b128 v[136:139], v119 offset:23056
	ds_read_b128 v[164:167], v121
	v_mfma_f32_32x32x16_bf16 v[2:17], v[148:151], v[144:147], v[2:17]
	ds_read_b128 v[144:147], v119 offset:20528
	ds_read_b128 v[180:183], v122
	v_mfma_f32_32x32x16_bf16 v[18:33], v[148:151], v[152:155], v[18:33]
	ds_read_b128 v[148:151], v119 offset:23088
	ds_read_b128 v[152:155], v123
	v_mfma_f32_32x32x16_bf16 v[34:49], v[156:159], v[168:171], v[34:49]
	s_waitcnt vmcnt(8)
	ds_write_b128 v116, v[66:69] offset:40976
	s_waitcnt vmcnt(7)
	ds_write_b128 v117, v[74:77] offset:40976
	v_mfma_f32_32x32x16_bf16 v[50:65], v[156:159], v[176:179], v[50:65]
	s_waitcnt vmcnt(6)
	ds_write_b128 v124, v[70:73]
	v_mfma_f32_32x32x16_bf16 v[2:17], v[172:175], v[168:171], v[2:17]
	v_mfma_f32_32x32x16_bf16 v[18:33], v[172:175], v[176:179], v[18:33]
	s_waitcnt lgkmcnt(0)
	s_barrier
; __device__ __forceinline__ void phase_gemm_bf16out(const bfr* A, int lda, int m0, int M, const bfr* Bt, int N, int K, bfr* C, int ldc, bfr* smem, int bid, int nb) {
;     ...
;         gp.mainloop(smem, al, bl);
;         const int un = u + nb;
;         if (un < nu) { al.init<256>(A, lda, m0 + (un / nt) * 256, m0 + M - 1, nullptr); bl.init<128>(Bt, K, (un % nt) * 128); gp.prefetch(al, bl); }
	v_mfma_f32_32x32x16_bf16 v[34:49], v[140:143], v[160:163], v[34:49]
	ds_read_b128 v[156:159], v119 offset:40976
	ds_read_b128 v[168:171], v125
	v_mfma_f32_32x32x16_bf16 v[50:65], v[140:143], v[164:167], v[50:65]
	ds_read_b128 v[140:143], v119 offset:43536
	ds_read_b128 v[172:175], v126
	v_mfma_f32_32x32x16_bf16 v[2:17], v[136:139], v[160:163], v[2:17]
	ds_read_b128 v[160:163], v119 offset:41008
	ds_read_b128 v[176:179], v127
	v_mfma_f32_32x32x16_bf16 v[18:33], v[136:139], v[164:167], v[18:33]
	ds_read_b128 v[136:139], v119 offset:43568
	ds_read_b128 v[164:167], v128
	v_mfma_f32_32x32x16_bf16 v[34:49], v[144:147], v[180:183], v[34:49]
	s_waitcnt vmcnt(5)
	ds_write_b128 v116, v[86:89] offset:16
	s_waitcnt vmcnt(4)
	ds_write_b128 v117, v[78:81] offset:16
	v_mfma_f32_32x32x16_bf16 v[50:65], v[144:147], v[152:155], v[50:65]
	s_waitcnt vmcnt(3)
	ds_write_b128 v116, v[82:85] offset:61456
	v_mfma_f32_32x32x16_bf16 v[2:17], v[148:151], v[180:183], v[2:17]
	v_mfma_f32_32x32x16_bf16 v[18:33], v[148:151], v[152:155], v[18:33]
	s_waitcnt lgkmcnt(0)
	s_barrier
	v_mfma_f32_32x32x16_bf16 v[34:49], v[156:159], v[168:171], v[34:49]
	ds_read_b128 v[144:147], v119 offset:16
	ds_read_b128 v[148:151], v129 offset:61456
	v_mfma_f32_32x32x16_bf16 v[50:65], v[156:159], v[172:175], v[50:65]
	ds_read_b128 v[152:155], v119 offset:2576
	ds_read_b128 v[156:159], v129 offset:64016
	v_mfma_f32_32x32x16_bf16 v[2:17], v[140:143], v[168:171], v[2:17]
	ds_read_b128 v[168:171], v119 offset:48
	ds_read_b128 v[180:183], v129 offset:61488
	v_mfma_f32_32x32x16_bf16 v[18:33], v[140:143], v[172:175], v[18:33]
	ds_read_b128 v[140:143], v119 offset:2608
	ds_read_b128 v[172:175], v130 offset:64016
	v_mfma_f32_32x32x16_bf16 v[34:49], v[160:163], v[176:179], v[34:49]
	s_waitcnt vmcnt(2)
	ds_write_b128 v116, v[98:101] offset:20496
	s_waitcnt vmcnt(1)
	ds_write_b128 v117, v[90:93] offset:20496
	v_mfma_f32_32x32x16_bf16 v[50:65], v[160:163], v[164:167], v[50:65]
	s_waitcnt vmcnt(0)
	ds_write_b128 v118, v[94:97]
	v_mfma_f32_32x32x16_bf16 v[2:17], v[136:139], v[176:179], v[2:17]
	v_mfma_f32_32x32x16_bf16 v[18:33], v[136:139], v[164:167], v[18:33]
	s_waitcnt lgkmcnt(0)
	s_barrier
	v_mfma_f32_32x32x16_bf16 v[34:49], v[144:147], v[148:151], v[34:49]
	ds_read_b128 v[136:139], v119 offset:20496
	ds_read_b128 v[160:163], v120
	v_mfma_f32_32x32x16_bf16 v[50:65], v[144:147], v[156:159], v[50:65]
	ds_read_b128 v[144:147], v119 offset:23056
	ds_read_b128 v[164:167], v121
	v_mfma_f32_32x32x16_bf16 v[2:17], v[152:155], v[148:151], v[2:17]
	ds_read_b128 v[148:151], v119 offset:20528
	ds_read_b128 v[176:179], v122
	v_mfma_f32_32x32x16_bf16 v[18:33], v[152:155], v[156:159], v[18:33]
	ds_read_b128 v[152:155], v119 offset:23088
	ds_read_b128 v[156:159], v123
	v_mfma_f32_32x32x16_bf16 v[34:49], v[168:171], v[180:183], v[34:49]
	v_mfma_f32_32x32x16_bf16 v[50:65], v[168:171], v[172:175], v[50:65]
	v_mfma_f32_32x32x16_bf16 v[2:17], v[140:143], v[180:183], v[2:17]
	v_mfma_f32_32x32x16_bf16 v[18:33], v[140:143], v[172:175], v[18:33]
	s_waitcnt lgkmcnt(0)
	s_barrier
	v_mfma_f32_32x32x16_bf16 v[34:49], v[136:139], v[160:163], v[34:49]
	v_mfma_f32_32x32x16_bf16 v[50:65], v[136:139], v[164:167], v[50:65]
	v_mfma_f32_32x32x16_bf16 v[2:17], v[144:147], v[160:163], v[2:17]
	v_mfma_f32_32x32x16_bf16 v[18:33], v[144:147], v[164:167], v[18:33]
	v_mfma_f32_32x32x16_bf16 v[34:49], v[148:151], v[176:179], v[34:49]
	v_mfma_f32_32x32x16_bf16 v[50:65], v[148:151], v[156:159], v[50:65]
	v_mfma_f32_32x32x16_bf16 v[2:17], v[152:155], v[176:179], v[2:17]
	v_mfma_f32_32x32x16_bf16 v[18:33], v[152:155], v[156:159], v[18:33]
	v_readlane_b32 s0, v253, 10
	s_add_i32 s13, s2, s0
	s_cmpk_lg_u32 s0, 0x100
	s_cbranch_scc1 .Lipx_u_10
	s_add_i32 s96, s96, 32
	s_mul_i32 s13, s96, 6554
	s_lshr_b32 s13, s13, 16
	s_mul_i32 s13, s13, 70
	s_add_i32 s13, s13, s96
	s_and_b32 s98, s44, 7
	s_mul_i32 s98, s98, 10
	s_add_i32 s13, s13, s98
.Lipx_u_10:
	v_readlane_b32 s1, v253, 11
	s_cmpk_gt_i32 s13, 0x289
	s_cselect_b64 s[0:1], -1, 0
	s_and_b64 vcc, exec, s[0:1]
	s_barrier
	s_cbranch_vccnz .LBB0_1744
	s_mul_hi_i32 s3, s13, 0x66666667
	s_lshr_b32 s4, s3, 31
	s_ashr_i32 s3, s3, 2
	s_add_i32 s3, s3, s4
	s_lshl_b32 s4, s3, 8
	v_or_b32_e32 v66, s4, v114
	v_ashrrev_i32_e32 v67, 31, v66
	v_lshlrev_b64 v[66:67], 11, v[66:67]
	v_lshl_add_u64 v[106:107], v[104:105], 0, v[66:67]
	v_or_b32_e32 v66, s4, v115
	v_ashrrev_i32_e32 v67, 31, v66
	s_mul_i32 s3, s3, 10
	v_lshlrev_b64 v[66:67], 11, v[66:67]
	s_sub_i32 s3, s13, s3
	v_lshl_add_u64 v[108:109], v[104:105], 0, v[66:67]
	v_lshl_or_b32 v66, s3, 7, v114
	v_ashrrev_i32_e32 v67, 31, v66
	v_lshlrev_b64 v[66:67], 11, v[66:67]
	v_lshl_add_u64 v[110:111], v[112:113], 0, v[66:67]
	global_load_dwordx4 v[78:81], v[108:109], off
	global_load_dwordx4 v[90:93], v[108:109], off offset:64
	global_load_dwordx4 v[82:85], v[110:111], off
	global_load_dwordx4 v[94:97], v[110:111], off offset:64
	global_load_dwordx4 v[98:101], v[106:107], off offset:64
	global_load_dwordx4 v[66:69], v[106:107], off offset:128
	global_load_dwordx4 v[74:77], v[108:109], off offset:128
	global_load_dwordx4 v[86:89], v[106:107], off
	global_load_dwordx4 v[70:73], v[110:111], off offset:128
